# K-loop heads aligned p2=6 +8 dwords; redundant setprio/waitcnt removed
# speedup vs baseline: 1.0066x; 1.0015x over previous
; template <class Epi, class Sched, bool ALIGN_EPI = false>
; __device__ __forceinline__ void gemm_phase(PG8_LAS unsigned char* lds, const Gemm g, const Sched& S, const Epi& E) {
;     ...
;         const char* nA = Sched::GATHER ? (const char*)g.A : (has_next ? (const char*)g.A + (size_t)nxt.pm * tstep : cA); const char* nB = has_next ? (const char*)g.Bt + nxt.boff + (size_t)nxt.pn * tstep : cB;
;         for (int t = 0; t < nt; t += 2) {
;             const bool last = (t == nt - 2);
;             const char* a1 = cA + (size_t)(t + 1) * kstep;
;             const char* a2 = last ? nA : cA + (size_t)(t + 2) * kstep; const char* b2 = last ? nB : cB + (size_t)(t + 2) * kstep;
;             const char* a3 = a2 + kstep; const char* b3 = b2 + kstep;
;             unsigned w0[2], w1[2];
; #pragma unroll
;             for (int i = 0; i < 2; ++i) { w0[i] = (Sched::GATHER && last) ? vn0[i] : vc0[i]; w1[i] = (Sched::GATHER && last) ? vn1[i] : vc1[i]; }
;             if (last && has_next) S.a_ready(nxt);
;             PG8_LDB(B0, 0, 0); PG8_LDB(B1, 0, 1); PG8_SCHED; PG8_LDA(At, 0, 0); PG8_STAGE(PG8_SA(1, 1), a1 + hstepA, vc1);
;             PG8_WAIT_V(8); PG8_WAIT_L(0); PG8_BAR; PG8_MMA(0, 0, At, B0); PG8_MMA(0, 1, At, B1); PG8_BAR; PG8_SCHED;
;             PG8_LDA(At, 0, 1); PG8_STAGE(PG8_SB(0, 0), b2, voffB); PG8_STAGE(PG8_SB(0, 1), b2 + hstep, voffB); PG8_STAGE(PG8_SA(0, 0), a2, w0);
;             PG8_WAIT_V(8); PG8_WAIT_L(0); PG8_BAR; PG8_MMA(1, 0, At, B0); PG8_MMA(1, 1, At, B1); PG8_BAR; PG8_SCHED;
;             PG8_LDB(B0, 1, 0); PG8_LDB(B1, 1, 1); PG8_SCHED; PG8_LDA(At, 1, 0); PG8_STAGE(PG8_SA(0, 1), a2 + hstepA, w1);
;             PG8_WAIT_V(8); PG8_WAIT_L(0); PG8_BAR; PG8_MMA(0, 0, At, B0); PG8_MMA(0, 1, At, B1); PG8_BAR; PG8_SCHED;
;             PG8_LDA(At, 1, 1); PG8_STAGE(PG8_SB(1, 0), b3, voffB); PG8_STAGE(PG8_SB(1, 1), b3 + hstep, voffB); PG8_STAGE(PG8_SA(1, 0), a3, w0);
;             PG8_WAIT_V(8); PG8_WAIT_L(0); PG8_BAR; PG8_MMA(1, 0, At, B0); PG8_MMA(1, 1, At, B1); PG8_BAR; PG8_SCHED;
;             if constexpr (Epi::KSCALE) { if (((t + 2) & 7) == 0 && t + 2 < nt) { E.kscale(acc, pf, ((t + 2) >> 3) - 1, wr, fr); PG8_SCHED; } }
;         }
;         if constexpr (ALIGN_EPI) { if (wr == 0) PG8_BAR; }
;         if constexpr (!Epi::AFTER_DRAIN) { E(acc, cur, wr, wc, fr, fq, pf); S.done(cur); }
;         if (!has_next) break;
; #pragma unroll
.LBB0_246:
	s_ashr_i32 s9, s8, 31
	s_lshl_b64 s[46:47], s[8:9], 20
	s_add_u32 s46, s40, s46
	s_addc_u32 s47, s41, s47
	s_and_b64 s[48:49], s[6:7], exec
	s_cselect_b32 s9, s47, s51
	s_cselect_b32 s76, s46, s50
	s_ashr_i32 s45, s44, 31
	s_lshl_b64 s[48:49], s[44:45], 20
	s_add_u32 s48, s3, s48
	s_addc_u32 s49, s35, s49
	s_and_b64 s[54:55], s[6:7], exec
	s_cselect_b32 s45, s49, s53
	s_cselect_b32 s77, s48, s52
	s_add_u32 s50, s50, 0x80080
	s_addc_u32 s51, s51, 0
	s_add_u32 s78, s52, 0x100
	v_mov_b32_e32 v2, 0
	s_addc_u32 s79, s53, 0
	s_mov_b32 s80, -2
	v_mov_b32_e32 v3, v2
	v_mov_b32_e32 v4, v2
	v_mov_b32_e32 v5, v2
	v_mov_b32_e32 v6, v2
	v_mov_b32_e32 v7, v2
	v_mov_b32_e32 v8, v2
	v_mov_b32_e32 v9, v2
	s_waitcnt vmcnt(0)
	v_mov_b32_e32 v18, v2
	v_mov_b32_e32 v19, v2
	v_mov_b32_e32 v20, v2
	v_mov_b32_e32 v21, v2
	v_mov_b32_e32 v22, v2
	v_mov_b32_e32 v23, v2
	v_mov_b32_e32 v24, v2
	v_mov_b32_e32 v25, v2
	v_mov_b32_e32 v34, v2
	v_mov_b32_e32 v35, v2
	v_mov_b32_e32 v36, v2
	v_mov_b32_e32 v37, v2
	v_mov_b32_e32 v38, v2
	v_mov_b32_e32 v39, v2
	v_mov_b32_e32 v40, v2
	v_mov_b32_e32 v41, v2
	v_mov_b32_e32 v50, v2
	v_mov_b32_e32 v51, v2
	v_mov_b32_e32 v52, v2
	v_mov_b32_e32 v53, v2
	v_mov_b32_e32 v54, v2
	v_mov_b32_e32 v55, v2
	v_mov_b32_e32 v56, v2
	v_mov_b32_e32 v57, v2
	v_mov_b32_e32 v66, v2
	v_mov_b32_e32 v67, v2
	v_mov_b32_e32 v68, v2
	v_mov_b32_e32 v69, v2
	v_mov_b32_e32 v70, v2
	v_mov_b32_e32 v71, v2
	v_mov_b32_e32 v72, v2
	v_mov_b32_e32 v73, v2
	v_mov_b32_e32 v82, v2
	v_mov_b32_e32 v83, v2
	v_mov_b32_e32 v84, v2
	v_mov_b32_e32 v85, v2
	v_mov_b32_e32 v86, v2
	v_mov_b32_e32 v87, v2
	v_mov_b32_e32 v88, v2
	v_mov_b32_e32 v89, v2
	v_mov_b32_e32 v98, v2
	v_mov_b32_e32 v99, v2
	v_mov_b32_e32 v100, v2
	v_mov_b32_e32 v101, v2
	v_mov_b32_e32 v102, v2
	v_mov_b32_e32 v103, v2
	v_mov_b32_e32 v104, v2
	v_mov_b32_e32 v105, v2
	v_mov_b32_e32 v114, v2
	v_mov_b32_e32 v115, v2
	v_mov_b32_e32 v116, v2
	v_mov_b32_e32 v117, v2
	v_mov_b32_e32 v118, v2
	v_mov_b32_e32 v119, v2
	v_mov_b32_e32 v120, v2
	v_mov_b32_e32 v121, v2
	v_mov_b32_e32 v74, v2
	v_mov_b32_e32 v75, v2
	v_mov_b32_e32 v76, v2
	v_mov_b32_e32 v77, v2
	v_mov_b32_e32 v78, v2
	v_mov_b32_e32 v79, v2
	v_mov_b32_e32 v80, v2
	v_mov_b32_e32 v81, v2
	v_mov_b32_e32 v90, v2
	v_mov_b32_e32 v91, v2
	v_mov_b32_e32 v92, v2
	v_mov_b32_e32 v93, v2
	v_mov_b32_e32 v94, v2
	v_mov_b32_e32 v95, v2
	v_mov_b32_e32 v96, v2
	v_mov_b32_e32 v97, v2
	v_mov_b32_e32 v106, v2
	v_mov_b32_e32 v107, v2
	v_mov_b32_e32 v108, v2
	v_mov_b32_e32 v109, v2
	v_mov_b32_e32 v110, v2
	v_mov_b32_e32 v111, v2
	v_mov_b32_e32 v112, v2
	v_mov_b32_e32 v113, v2
	v_mov_b32_e32 v122, v2
	v_mov_b32_e32 v123, v2
	v_mov_b32_e32 v124, v2
	v_mov_b32_e32 v125, v2
	v_mov_b32_e32 v126, v2
	v_mov_b32_e32 v127, v2
	v_mov_b32_e32 v128, v2
	v_mov_b32_e32 v129, v2
	v_mov_b32_e32 v58, v2
	v_mov_b32_e32 v59, v2
	v_mov_b32_e32 v60, v2
	v_mov_b32_e32 v61, v2
	v_mov_b32_e32 v62, v2
	v_mov_b32_e32 v63, v2
	v_mov_b32_e32 v64, v2
	v_mov_b32_e32 v65, v2
	v_mov_b32_e32 v42, v2
	v_mov_b32_e32 v43, v2
	v_mov_b32_e32 v44, v2
	v_mov_b32_e32 v45, v2
	v_mov_b32_e32 v46, v2
	v_mov_b32_e32 v47, v2
	v_mov_b32_e32 v48, v2
	v_mov_b32_e32 v49, v2
	v_mov_b32_e32 v26, v2
	v_mov_b32_e32 v27, v2
	v_mov_b32_e32 v28, v2
	v_mov_b32_e32 v29, v2
	v_mov_b32_e32 v30, v2
	v_mov_b32_e32 v31, v2
	v_mov_b32_e32 v32, v2
	v_mov_b32_e32 v33, v2
	v_mov_b32_e32 v10, v2
	v_mov_b32_e32 v11, v2
	v_mov_b32_e32 v12, v2
	v_mov_b32_e32 v13, v2
	v_mov_b32_e32 v14, v2
	v_mov_b32_e32 v15, v2
	v_mov_b32_e32 v16, v2
	v_mov_b32_e32 v17, v2
	.p2align 6
	s_nop 0
	s_nop 0
	s_nop 0
	s_nop 0
	s_nop 0
	s_nop 0
	s_nop 0
	s_nop 0

; template <class Epi, class Sched, bool ALIGN_EPI = false>
; __device__ __forceinline__ void gemm_phase(PG8_LAS unsigned char* lds, const Gemm g, const Sched& S, const Epi& E) {
;     ...
;         const char* nA = Sched::GATHER ? (const char*)g.A : (has_next ? (const char*)g.A + (size_t)nxt.pm * tstep : cA); const char* nB = has_next ? (const char*)g.Bt + nxt.boff + (size_t)nxt.pn * tstep : cB;
;         for (int t = 0; t < nt; t += 2) {
;             const bool last = (t == nt - 2);
;             const char* a1 = cA + (size_t)(t + 1) * kstep;
;             const char* a2 = last ? nA : cA + (size_t)(t + 2) * kstep; const char* b2 = last ? nB : cB + (size_t)(t + 2) * kstep;
;             const char* a3 = a2 + kstep; const char* b3 = b2 + kstep;
;             unsigned w0[2], w1[2];
; #pragma unroll
;             for (int i = 0; i < 2; ++i) { w0[i] = (Sched::GATHER && last) ? vn0[i] : vc0[i]; w1[i] = (Sched::GATHER && last) ? vn1[i] : vc1[i]; }
;             if (last && has_next) S.a_ready(nxt);
;             PG8_LDB(B0, 0, 0); PG8_LDB(B1, 0, 1); PG8_SCHED; PG8_LDA(At, 0, 0); PG8_STAGE(PG8_SA(1, 1), a1 + hstepA, vc1);
;             PG8_WAIT_V(8); PG8_WAIT_L(0); PG8_BAR; PG8_MMA(0, 0, At, B0); PG8_MMA(0, 1, At, B1); PG8_BAR; PG8_SCHED;
;             PG8_LDA(At, 0, 1); PG8_STAGE(PG8_SB(0, 0), b2, voffB); PG8_STAGE(PG8_SB(0, 1), b2 + hstep, voffB); PG8_STAGE(PG8_SA(0, 0), a2, w0);
;             PG8_WAIT_V(8); PG8_WAIT_L(0); PG8_BAR; PG8_MMA(1, 0, At, B0); PG8_MMA(1, 1, At, B1); PG8_BAR; PG8_SCHED;
;             PG8_LDB(B0, 1, 0); PG8_LDB(B1, 1, 1); PG8_SCHED; PG8_LDA(At, 1, 0); PG8_STAGE(PG8_SA(0, 1), a2 + hstepA, w1);
;             PG8_WAIT_V(8); PG8_WAIT_L(0); PG8_BAR; PG8_MMA(0, 0, At, B0); PG8_MMA(0, 1, At, B1); PG8_BAR; PG8_SCHED;
;             PG8_LDA(At, 1, 1); PG8_STAGE(PG8_SB(1, 0), b3, voffB); PG8_STAGE(PG8_SB(1, 1), b3 + hstep, voffB); PG8_STAGE(PG8_SA(1, 0), a3, w0);
;             PG8_WAIT_V(8); PG8_WAIT_L(0); PG8_BAR; PG8_MMA(1, 0, At, B0); PG8_MMA(1, 1, At, B1); PG8_BAR; PG8_SCHED;
;             if constexpr (Epi::KSCALE) { if (((t + 2) & 7) == 0 && t + 2 < nt) { E.kscale(acc, pf, ((t + 2) >> 3) - 1, wr, fr); PG8_SCHED; } }
;         }
;         if constexpr (ALIGN_EPI) { if (wr == 0) PG8_BAR; }
;         if constexpr (!Epi::AFTER_DRAIN) { E(acc, cur, wr, wc, fr, fq, pf); S.done(cur); }
;         if (!has_next) break;
; #pragma unroll
.LBB0_502:
	s_ashr_i32 s47, s46, 31
	s_lshl_b64 s[10:11], s[46:47], 20
	s_add_u32 s10, s3, s10
	s_addc_u32 s11, s35, s11
	s_and_b64 s[12:13], s[8:9], exec
	s_cselect_b32 s47, s11, s51
	s_cselect_b32 s49, s10, s50
	s_ashr_i32 s45, s44, 31
	s_lshl_b64 s[12:13], s[44:45], 20
	s_add_u32 s12, s58, s12
	s_addc_u32 s13, s59, s13
	s_and_b64 s[54:55], s[8:9], exec
	v_mov_b32_e32 v4, v2
	v_mov_b32_e32 v5, v2
	s_cselect_b32 s45, s13, s53
	s_cselect_b32 s78, s12, s52
	s_add_i32 s54, s76, s72
	v_mov_b32_e32 v3, v2
	v_mov_b64_e32 v[14:15], v[4:5]
	v_mov_b64_e32 v[18:19], v[4:5]
	v_mov_b64_e32 v[30:31], v[4:5]
	v_mov_b64_e32 v[34:35], v[4:5]
	v_mov_b64_e32 v[46:47], v[4:5]
	v_mov_b64_e32 v[50:51], v[4:5]
	v_mov_b64_e32 v[62:63], v[4:5]
	v_mov_b64_e32 v[66:67], v[4:5]
	v_mov_b64_e32 v[70:71], v[4:5]
	v_mov_b64_e32 v[74:75], v[4:5]
	v_mov_b64_e32 v[86:87], v[4:5]
	v_mov_b64_e32 v[90:91], v[4:5]
	v_mov_b64_e32 v[102:103], v[4:5]
	v_mov_b64_e32 v[106:107], v[4:5]
	v_mov_b64_e32 v[110:111], v[4:5]
	v_mov_b64_e32 v[118:119], v[4:5]
	v_mov_b64_e32 v[78:79], v[4:5]
	v_mov_b64_e32 v[82:83], v[4:5]
	v_mov_b64_e32 v[94:95], v[4:5]
	v_mov_b64_e32 v[98:99], v[4:5]
	v_mov_b64_e32 v[114:115], v[4:5]
	v_mov_b64_e32 v[122:123], v[4:5]
	v_mov_b64_e32 v[126:127], v[4:5]
	v_mov_b64_e32 v[130:131], v[4:5]
	v_mov_b64_e32 v[58:59], v[4:5]
	v_mov_b64_e32 v[54:55], v[4:5]
	v_mov_b64_e32 v[42:43], v[4:5]
	v_mov_b64_e32 v[38:39], v[4:5]
	v_mov_b64_e32 v[26:27], v[4:5]
	v_mov_b64_e32 v[22:23], v[4:5]
	v_mov_b64_e32 v[10:11], v[4:5]
	s_add_u32 s79, s52, 0x100
	v_mov_b64_e32 v[12:13], v[2:3]
	v_mov_b64_e32 v[16:17], v[2:3]
	v_mov_b64_e32 v[28:29], v[2:3]
	v_mov_b64_e32 v[32:33], v[2:3]
	v_mov_b64_e32 v[44:45], v[2:3]
	v_mov_b64_e32 v[48:49], v[2:3]
	v_mov_b64_e32 v[60:61], v[2:3]
	v_mov_b64_e32 v[64:65], v[2:3]
	v_mov_b64_e32 v[68:69], v[2:3]
	v_mov_b64_e32 v[72:73], v[2:3]
	v_mov_b64_e32 v[84:85], v[2:3]
	v_mov_b64_e32 v[88:89], v[2:3]
	v_mov_b64_e32 v[100:101], v[2:3]
	v_mov_b64_e32 v[104:105], v[2:3]
	v_mov_b64_e32 v[108:109], v[2:3]
	v_mov_b64_e32 v[116:117], v[2:3]
	v_mov_b64_e32 v[76:77], v[2:3]
	v_mov_b64_e32 v[80:81], v[2:3]
	v_mov_b64_e32 v[92:93], v[2:3]
	v_mov_b64_e32 v[96:97], v[2:3]
	v_mov_b64_e32 v[112:113], v[2:3]
	v_mov_b64_e32 v[120:121], v[2:3]
	v_mov_b64_e32 v[124:125], v[2:3]
	v_mov_b64_e32 v[128:129], v[2:3]
	v_mov_b64_e32 v[56:57], v[2:3]
	v_mov_b64_e32 v[52:53], v[2:3]
	v_mov_b64_e32 v[40:41], v[2:3]
	v_mov_b64_e32 v[36:37], v[2:3]
	v_mov_b64_e32 v[24:25], v[2:3]
	v_mov_b64_e32 v[20:21], v[2:3]
	v_mov_b64_e32 v[8:9], v[2:3]
	v_mov_b64_e32 v[6:7], v[4:5]
	v_add_u32_e32 v137, s54, v176
	v_lshl_add_u64 v[132:133], s[50:51], 0, v[154:155]
	v_lshl_add_u64 v[134:135], s[50:51], 0, v[156:157]
	s_addc_u32 s80, s53, 0
	s_mov_b32 s81, 0
	s_mov_b64 s[52:53], 0
	v_mov_b64_e32 v[4:5], v[2:3]
	s_branch .LBB0_504
	.p2align 6
	s_nop 0
	s_nop 0
	s_nop 0
	s_nop 0
	s_nop 0
	s_nop 0
	s_nop 0
	s_nop 0

; template <class Epi, class Sched, bool ALIGN_EPI = false>
; __device__ __forceinline__ void gemm_phase(PG8_LAS unsigned char* lds, const Gemm g, const Sched& S, const Epi& E) {
;     ...
;         const char* nA = Sched::GATHER ? (const char*)g.A : (has_next ? (const char*)g.A + (size_t)nxt.pm * tstep : cA); const char* nB = has_next ? (const char*)g.Bt + nxt.boff + (size_t)nxt.pn * tstep : cB;
;         for (int t = 0; t < nt; t += 2) {
;             const bool last = (t == nt - 2);
;             const char* a1 = cA + (size_t)(t + 1) * kstep;
;             const char* a2 = last ? nA : cA + (size_t)(t + 2) * kstep; const char* b2 = last ? nB : cB + (size_t)(t + 2) * kstep;
;             const char* a3 = a2 + kstep; const char* b3 = b2 + kstep;
;             unsigned w0[2], w1[2];
; #pragma unroll
;             for (int i = 0; i < 2; ++i) { w0[i] = (Sched::GATHER && last) ? vn0[i] : vc0[i]; w1[i] = (Sched::GATHER && last) ? vn1[i] : vc1[i]; }
;             if (last && has_next) S.a_ready(nxt);
;             PG8_LDB(B0, 0, 0); PG8_LDB(B1, 0, 1); PG8_SCHED; PG8_LDA(At, 0, 0); PG8_STAGE(PG8_SA(1, 1), a1 + hstepA, vc1);
;             PG8_WAIT_V(8); PG8_WAIT_L(0); PG8_BAR; PG8_MMA(0, 0, At, B0); PG8_MMA(0, 1, At, B1); PG8_BAR; PG8_SCHED;
;             PG8_LDA(At, 0, 1); PG8_STAGE(PG8_SB(0, 0), b2, voffB); PG8_STAGE(PG8_SB(0, 1), b2 + hstep, voffB); PG8_STAGE(PG8_SA(0, 0), a2, w0);
;             PG8_WAIT_V(8); PG8_WAIT_L(0); PG8_BAR; PG8_MMA(1, 0, At, B0); PG8_MMA(1, 1, At, B1); PG8_BAR; PG8_SCHED;
;             PG8_LDB(B0, 1, 0); PG8_LDB(B1, 1, 1); PG8_SCHED; PG8_LDA(At, 1, 0); PG8_STAGE(PG8_SA(0, 1), a2 + hstepA, w1);
;             PG8_WAIT_V(8); PG8_WAIT_L(0); PG8_BAR; PG8_MMA(0, 0, At, B0); PG8_MMA(0, 1, At, B1); PG8_BAR; PG8_SCHED;
;             PG8_LDA(At, 1, 1); PG8_STAGE(PG8_SB(1, 0), b3, voffB); PG8_STAGE(PG8_SB(1, 1), b3 + hstep, voffB); PG8_STAGE(PG8_SA(1, 0), a3, w0);
;             PG8_WAIT_V(8); PG8_WAIT_L(0); PG8_BAR; PG8_MMA(1, 0, At, B0); PG8_MMA(1, 1, At, B1); PG8_BAR; PG8_SCHED;
;             if constexpr (Epi::KSCALE) { if (((t + 2) & 7) == 0 && t + 2 < nt) { E.kscale(acc, pf, ((t + 2) >> 3) - 1, wr, fr); PG8_SCHED; } }
;         }
;         if constexpr (ALIGN_EPI) { if (wr == 0) PG8_BAR; }
;         if constexpr (!Epi::AFTER_DRAIN) { E(acc, cur, wr, wc, fr, fq, pf); S.done(cur); }
;         if (!has_next) break;
; #pragma unroll
.LBB0_720:
	v_mov_b32_e32 v153, v135
	v_mov_b32_e32 v155, v135
	s_add_u32 s49, s56, 0x100
	v_mov_b32_e32 v26, 0
	s_addc_u32 s89, s57, 0
	v_lshl_add_u64 v[158:159], s[40:41], 0, v[154:155]
	v_lshl_add_u64 v[160:161], s[40:41], 0, v[152:153]
	s_mov_b32 s90, -2
	s_mov_b64 s[56:57], 0
	v_mov_b32_e32 v27, v26
	v_mov_b32_e32 v28, v26
	v_mov_b32_e32 v29, v26
	v_mov_b32_e32 v38, v26
	v_mov_b32_e32 v39, v26
	v_mov_b32_e32 v40, v26
	v_mov_b32_e32 v41, v26
	v_mov_b32_e32 v46, v26
	v_mov_b32_e32 v47, v26
	v_mov_b32_e32 v48, v26
	v_mov_b32_e32 v49, v26
	v_mov_b32_e32 v54, v26
	v_mov_b32_e32 v55, v26
	v_mov_b32_e32 v56, v26
	v_mov_b32_e32 v57, v26
	v_mov_b32_e32 v2, v26
	v_mov_b32_e32 v3, v26
	v_mov_b32_e32 v4, v26
	v_mov_b32_e32 v5, v26
	v_mov_b32_e32 v14, v26
	v_mov_b32_e32 v15, v26
	v_mov_b32_e32 v16, v26
	v_mov_b32_e32 v17, v26
	v_mov_b32_e32 v30, v26
	v_mov_b32_e32 v31, v26
	v_mov_b32_e32 v32, v26
	v_mov_b32_e32 v33, v26
	v_mov_b32_e32 v34, v26
	v_mov_b32_e32 v35, v26
	v_mov_b32_e32 v36, v26
	v_mov_b32_e32 v37, v26
	v_mov_b32_e32 v42, v26
	v_mov_b32_e32 v43, v26
	v_mov_b32_e32 v44, v26
	v_mov_b32_e32 v45, v26
	v_mov_b32_e32 v50, v26
	v_mov_b32_e32 v51, v26
	v_mov_b32_e32 v52, v26
	v_mov_b32_e32 v53, v26
	v_mov_b32_e32 v58, v26
	v_mov_b32_e32 v59, v26
	v_mov_b32_e32 v60, v26
	v_mov_b32_e32 v61, v26
	v_mov_b32_e32 v62, v26
	v_mov_b32_e32 v63, v26
	v_mov_b32_e32 v64, v26
	v_mov_b32_e32 v65, v26
	v_mov_b32_e32 v66, v26
	v_mov_b32_e32 v67, v26
	v_mov_b32_e32 v68, v26
	v_mov_b32_e32 v69, v26
	v_mov_b32_e32 v70, v26
	v_mov_b32_e32 v71, v26
	v_mov_b32_e32 v72, v26
	v_mov_b32_e32 v73, v26
	v_mov_b32_e32 v82, v26
	v_mov_b32_e32 v83, v26
	v_mov_b32_e32 v84, v26
	v_mov_b32_e32 v85, v26
	v_mov_b32_e32 v86, v26
	v_mov_b32_e32 v87, v26
	v_mov_b32_e32 v88, v26
	v_mov_b32_e32 v89, v26
	v_mov_b32_e32 v98, v26
	v_mov_b32_e32 v99, v26
	v_mov_b32_e32 v100, v26
	v_mov_b32_e32 v101, v26
	v_mov_b32_e32 v102, v26
	v_mov_b32_e32 v103, v26
	v_mov_b32_e32 v104, v26
	v_mov_b32_e32 v105, v26
	v_mov_b32_e32 v114, v26
	v_mov_b32_e32 v115, v26
	v_mov_b32_e32 v116, v26
	v_mov_b32_e32 v117, v26
	v_mov_b32_e32 v118, v26
	v_mov_b32_e32 v119, v26
	v_mov_b32_e32 v120, v26
	v_mov_b32_e32 v121, v26
	v_mov_b32_e32 v74, v26
	v_mov_b32_e32 v75, v26
	v_mov_b32_e32 v76, v26
	v_mov_b32_e32 v77, v26
	v_mov_b32_e32 v78, v26
	v_mov_b32_e32 v79, v26
	v_mov_b32_e32 v80, v26
	v_mov_b32_e32 v81, v26
	v_mov_b32_e32 v90, v26
	v_mov_b32_e32 v91, v26
	v_mov_b32_e32 v92, v26
	v_mov_b32_e32 v93, v26
	v_mov_b32_e32 v94, v26
	v_mov_b32_e32 v95, v26
	v_mov_b32_e32 v96, v26
	v_mov_b32_e32 v97, v26
	v_mov_b32_e32 v106, v26
	v_mov_b32_e32 v107, v26
	v_mov_b32_e32 v108, v26
	v_mov_b32_e32 v109, v26
	v_mov_b32_e32 v110, v26
	v_mov_b32_e32 v111, v26
	v_mov_b32_e32 v112, v26
	v_mov_b32_e32 v113, v26
	v_mov_b32_e32 v122, v26
	v_mov_b32_e32 v123, v26
	v_mov_b32_e32 v124, v26
	v_mov_b32_e32 v125, v26
	v_mov_b32_e32 v126, v26
	v_mov_b32_e32 v127, v26
	v_mov_b32_e32 v128, v26
	v_mov_b32_e32 v129, v26
	v_mov_b32_e32 v22, v26
	v_mov_b32_e32 v23, v26
	v_mov_b32_e32 v24, v26
	v_mov_b32_e32 v25, v26
	v_mov_b32_e32 v18, v26
	v_mov_b32_e32 v19, v26
	v_mov_b32_e32 v20, v26
	v_mov_b32_e32 v21, v26
	v_mov_b32_e32 v10, v26
	v_mov_b32_e32 v11, v26
	v_mov_b32_e32 v12, v26
	v_mov_b32_e32 v13, v26
	v_mov_b32_e32 v6, v26
	v_mov_b32_e32 v7, v26
	v_mov_b32_e32 v8, v26
	v_mov_b32_e32 v9, v26
	.p2align 6
	s_nop 0
	s_nop 0
	s_nop 0
	s_nop 0
	s_nop 0
	s_nop 0
	s_nop 0
	s_nop 0

; #define PG8_STAGE(bufoff, gbase, voff) do { _Pragma("unroll") for (int _i = 0; _i < 2; ++_i) \
;         __builtin_amdgcn_global_load_lds((const unsigned*)((const char*)(gbase) + (voff)[_i]), (PG8_LAS unsigned*)(lds + (bufoff) + ldsw + _i * 8192), 16, 0, 0); } while (0)
; #define PG8_WAIT_V(n) asm volatile("s_waitcnt vmcnt(" #n ")" ::: "memory")
; #define PG8_BAR __builtin_amdgcn_s_barrier()
;     __device__ __forceinline__ Pre pre(const Unit& u, int wr, int fr) const { Pre p; const int rl0 = wr * 64 + fr;
; #pragma unroll
;         for (int ai = 0; ai < 2; ++ai)
; #pragma unroll
;             for (int m = 0; m < 4; ++m) { int slot = u.s0 + rl0 + ai * HALF + m * 16; slot = slot < u.cnt ? slot : u.cnt - 1; p.rs[ai][m] = lrs[u.e * 16384 + slot]; }
;         return p; }
; template <class Epi, class Sched, bool ALIGN_EPI = false>
; __device__ __forceinline__ void gemm_phase(PG8_LAS unsigned char* lds, const Gemm g, const Sched& S, const Epi& E) {
;     ...
;     PG8_STAGE(PG8_SB(0, 0), cB, voffB); PG8_STAGE(PG8_SB(0, 1), cB + hstep, voffB); PG8_STAGE(PG8_SA(0, 0), cA, vc0); PG8_STAGE(PG8_SA(0, 1), cA + hstepA, vc1);
;     if (wr == 1) PG8_BAR;
;     PG8_WAIT_V(2); PG8_BAR;
;     PG8_STAGE(PG8_SB(1, 0), cB + kstep, voffB); PG8_STAGE(PG8_SA(1, 0), cA + kstep, vc0); PG8_STAGE(PG8_SB(1, 1), cB + hstep + kstep, voffB);
;     PG8_WAIT_V(6); PG8_BAR;
.LBB0_786:
	s_add_u32 s22, s36, 0x30800000
	v_lshlrev_b32_e32 v9, 2, v162
	s_addc_u32 s23, s37, 0
	v_lshl_or_b32 v166, s15, 6, v162
	v_lshl_or_b32 v8, v162, 6, v163
	s_lshl_b32 s15, s15, 13
	v_and_b32_e32 v9, 32, v9
	s_lshl_b32 s14, s14, 5
	v_bitop3_b32 v20, v8, s15, v9 bitop3:0xde
	s_and_b32 s42, s14, 0x60
	s_mov_b64 s[14:15], 0x80
	s_add_i32 m0, s27, 0x18000
	v_lshl_add_u64 v[4:5], v[4:5], 0, s[14:15]
	s_waitcnt vmcnt(2)
	s_barrier
	global_load_lds_dwordx4 v[4:5], off
	s_add_i32 m0, s27, 0x1a000
	s_add_u32 s50, s36, 0x3c800080
	v_lshl_add_u64 v[2:3], v[2:3], 0, s[14:15]
	s_addc_u32 s51, s37, 0
	s_add_i32 s43, s27, 0x8000
	global_load_lds_dwordx4 v[2:3], off
	v_lshl_add_u64 v[2:3], s[50:51], 0, v[148:149]
	s_mov_b32 m0, s43
	s_add_i32 s44, s27, 0xa000
	global_load_lds_dwordx4 v[2:3], off
	v_lshl_add_u64 v[2:3], s[50:51], 0, v[150:151]
	s_add_u32 s50, s12, 0x80080
	s_mov_b32 m0, s44
	s_addc_u32 s51, s13, 0
	global_load_lds_dwordx4 v[2:3], off
	s_add_i32 m0, s27, 0x1c000
	v_lshl_add_u64 v[2:3], s[50:51], 0, v[146:147]
	global_load_lds_dwordx4 v[2:3], off
	v_lshl_add_u64 v[2:3], s[50:51], 0, v[144:145]
	s_add_i32 m0, s27, 0x1e000
	v_add_u32_e32 v18, s48, v166
	global_load_lds_dwordx4 v[2:3], off
	v_min_i32_e32 v2, s46, v18
	v_add_u32_e32 v4, 16, v18
	v_add_u32_e32 v8, 32, v18
	v_add_u32_e32 v10, 48, v18
	v_add_u32_e32 v12, 0x80, v18
	v_add_u32_e32 v14, 0x90, v18
	v_add_u32_e32 v16, 0xa0, v18
	v_add_u32_e32 v18, 0xb0, v18
	v_add_u32_e32 v2, s45, v2
	v_min_i32_e32 v4, s46, v4
	v_min_i32_e32 v8, s46, v8
	v_min_i32_e32 v10, s46, v10
	v_min_i32_e32 v12, s46, v12
	v_min_i32_e32 v14, s46, v14
	v_min_i32_e32 v16, s46, v16
	v_min_i32_e32 v18, s46, v18
	v_ashrrev_i32_e32 v3, 31, v2
	v_add_u32_e32 v4, s45, v4
	v_add_u32_e32 v8, s45, v8
	v_add_u32_e32 v10, s45, v10
	v_add_u32_e32 v12, s45, v12
	v_add_u32_e32 v14, s45, v14
	v_add_u32_e32 v16, s45, v16
	v_add_u32_e32 v18, s45, v18
	v_lshl_add_u64 v[2:3], v[2:3], 2, s[22:23]
	v_ashrrev_i32_e32 v5, 31, v4
	v_ashrrev_i32_e32 v9, 31, v8
	v_ashrrev_i32_e32 v11, 31, v10
	v_ashrrev_i32_e32 v13, 31, v12
	v_ashrrev_i32_e32 v15, 31, v14
	v_ashrrev_i32_e32 v17, 31, v16
	v_ashrrev_i32_e32 v19, 31, v18
	s_waitcnt vmcnt(6)
	s_barrier
;     __device__ __forceinline__ Pre pre(const Unit& u, int wr, int fr) const { Pre p; const int rl0 = wr * 64 + fr;
; #pragma unroll
;         for (int ai = 0; ai < 2; ++ai)
; #pragma unroll
;             for (int m = 0; m < 4; ++m) { int slot = u.s0 + rl0 + ai * HALF + m * 16; slot = slot < u.cnt ? slot : u.cnt - 1; p.rs[ai][m] = lrs[u.e * 16384 + slot]; }
;         return p; }
; template <class Epi, class Sched, bool ALIGN_EPI = false>
; __device__ __forceinline__ void gemm_phase(PG8_LAS unsigned char* lds, const Gemm g, const Sched& S, const Epi& E) {
;     ...
;     Unit cur, nxt; int ui = 0;
;     if (!S.next(0, cur)) return;
;     f32x4 acc[2][2][4][2];
; #pragma unroll
;     for (int a = 0; a < 2; ++a)
; #pragma unroll
;         for (int b = 0; b < 2; ++b)
; #pragma unroll
;             for (int m = 0; m < 4; ++m)
; #pragma unroll
;                 for (int n = 0; n < 2; ++n) acc[a][b][m][n] = (f32x4){0.f, 0.f, 0.f, 0.f};
	v_lshl_add_u64 v[4:5], v[4:5], 2, s[22:23]
	v_lshl_add_u64 v[8:9], v[8:9], 2, s[22:23]
	v_lshl_add_u64 v[10:11], v[10:11], 2, s[22:23]
	v_lshl_add_u64 v[12:13], v[12:13], 2, s[22:23]
	v_lshl_add_u64 v[14:15], v[14:15], 2, s[22:23]
	v_lshl_add_u64 v[16:17], v[16:17], 2, s[22:23]
	v_lshl_add_u64 v[18:19], v[18:19], 2, s[22:23]
	global_load_dword v156, v[2:3], off
	global_load_dword v142, v[4:5], off
	global_load_dword v140, v[8:9], off
	global_load_dword v138, v[10:11], off
	global_load_dword v136, v[12:13], off
	global_load_dword v134, v[14:15], off
	global_load_dword v132, v[16:17], off
	global_load_dword v130, v[18:19], off
	s_add_u32 s16, s16, s47
	s_addc_u32 s17, s17, 0
	s_add_u32 s45, s16, 0x4800100
	v_lshl_or_b32 v21, s42, 7, v164
	s_mov_b64 s[18:19], 0x3c800080
	s_addc_u32 s46, s17, 0
	v_add3_u32 v2, v1, v7, v141
	v_mov_b32_e32 v3, v147
	s_add_i32 s50, 0, 0x10000
	s_add_i32 s52, 0, 0x14000
	s_add_i32 s54, 0, 0x18000
	s_add_i32 s16, 0, 0x1c000
	v_lshl_add_u64 v[158:159], v[2:3], 0, s[18:19]
	v_add3_u32 v2, v1, v6, v141
	v_add_u32_e32 v167, s50, v21
	v_add_u32_e32 v168, s52, v21
	s_add_i32 s50, s50, s56
	s_add_i32 s52, s52, s56
	v_add_u32_e32 v170, s54, v21
	s_add_i32 s54, s54, s56
	s_add_i32 s56, s16, s56
	v_mov_b32_e32 v153, v147
	v_mov_b32_e32 v155, v147
	v_lshl_add_u64 v[160:161], v[2:3], 0, s[18:19]
	s_mov_b32 s47, -2
	v_add_u32_e32 v169, 0, v20
	s_add_i32 s48, s27, 0xc000
	s_add_i32 s49, s27, 0xe000
	s_add_i32 s51, s50, 0x2000
	s_add_i32 s53, s52, 0x2000
	v_add_u32_e32 v171, s16, v21
	s_add_i32 s55, s54, 0x2000
	s_add_i32 s57, s56, 0x2000
	s_mov_b64 s[16:17], s[36:37]
	v_mov_b32_e32 v30, v147
	v_mov_b32_e32 v31, v147
	v_mov_b32_e32 v32, v147
	v_mov_b32_e32 v33, v147
	v_mov_b32_e32 v38, v147
	v_mov_b32_e32 v39, v147
	v_mov_b32_e32 v40, v147
	v_mov_b32_e32 v41, v147
	v_mov_b32_e32 v46, v147
	v_mov_b32_e32 v47, v147
	v_mov_b32_e32 v48, v147
	v_mov_b32_e32 v49, v147
	v_mov_b32_e32 v54, v147
	v_mov_b32_e32 v55, v147
	v_mov_b32_e32 v56, v147
	v_mov_b32_e32 v57, v147
	v_mov_b32_e32 v2, v147
	v_mov_b32_e32 v4, v147
	v_mov_b32_e32 v5, v147
	v_mov_b32_e32 v14, v147
	v_mov_b32_e32 v15, v147
	v_mov_b32_e32 v16, v147
	v_mov_b32_e32 v17, v147
	v_mov_b32_e32 v26, v147
	v_mov_b32_e32 v27, v147
	v_mov_b32_e32 v28, v147
	v_mov_b32_e32 v29, v147
	v_mov_b32_e32 v34, v147
	v_mov_b32_e32 v35, v147
	v_mov_b32_e32 v36, v147
	v_mov_b32_e32 v37, v147
	v_mov_b32_e32 v42, v147
	v_mov_b32_e32 v43, v147
	v_mov_b32_e32 v44, v147
	v_mov_b32_e32 v45, v147
	v_mov_b32_e32 v50, v147
	v_mov_b32_e32 v51, v147
	v_mov_b32_e32 v52, v147
	v_mov_b32_e32 v53, v147
	v_mov_b32_e32 v58, v147
	v_mov_b32_e32 v59, v147
	v_mov_b32_e32 v60, v147
	v_mov_b32_e32 v61, v147
	v_mov_b32_e32 v62, v147
	v_mov_b32_e32 v63, v147
	v_mov_b32_e32 v64, v147
	v_mov_b32_e32 v65, v147
	v_mov_b32_e32 v66, v147
	v_mov_b32_e32 v67, v147
	v_mov_b32_e32 v68, v147
	v_mov_b32_e32 v69, v147
	v_mov_b32_e32 v70, v147
	v_mov_b32_e32 v71, v147
	v_mov_b32_e32 v72, v147
	v_mov_b32_e32 v73, v147
	v_mov_b32_e32 v82, v147
	v_mov_b32_e32 v83, v147
	v_mov_b32_e32 v84, v147
	v_mov_b32_e32 v85, v147
	v_mov_b32_e32 v86, v147
	v_mov_b32_e32 v87, v147
	v_mov_b32_e32 v88, v147
	v_mov_b32_e32 v89, v147
	v_mov_b32_e32 v98, v147
	v_mov_b32_e32 v99, v147
	v_mov_b32_e32 v100, v147
	v_mov_b32_e32 v101, v147
	v_mov_b32_e32 v102, v147
	v_mov_b32_e32 v103, v147
	v_mov_b32_e32 v104, v147
	v_mov_b32_e32 v105, v147
	v_mov_b32_e32 v114, v147
	v_mov_b32_e32 v115, v147
	v_mov_b32_e32 v116, v147
	v_mov_b32_e32 v117, v147
	v_mov_b32_e32 v118, v147
	v_mov_b32_e32 v119, v147
	v_mov_b32_e32 v120, v147
	v_mov_b32_e32 v121, v147
	v_mov_b32_e32 v74, v147
	v_mov_b32_e32 v75, v147
	v_mov_b32_e32 v76, v147
	v_mov_b32_e32 v77, v147
	v_mov_b32_e32 v78, v147
	v_mov_b32_e32 v79, v147
	v_mov_b32_e32 v80, v147
	v_mov_b32_e32 v81, v147
	v_mov_b32_e32 v90, v147
	v_mov_b32_e32 v91, v147
	v_mov_b32_e32 v92, v147
	v_mov_b32_e32 v93, v147
	v_mov_b32_e32 v94, v147
	v_mov_b32_e32 v95, v147
	v_mov_b32_e32 v96, v147
	v_mov_b32_e32 v97, v147
	v_mov_b32_e32 v106, v147
	v_mov_b32_e32 v107, v147
	v_mov_b32_e32 v108, v147
	v_mov_b32_e32 v109, v147
	v_mov_b32_e32 v110, v147
	v_mov_b32_e32 v111, v147
	v_mov_b32_e32 v112, v147
	v_mov_b32_e32 v113, v147
	v_mov_b32_e32 v122, v147
	v_mov_b32_e32 v123, v147
	v_mov_b32_e32 v124, v147
	v_mov_b32_e32 v125, v147
	v_mov_b32_e32 v126, v147
	v_mov_b32_e32 v127, v147
	v_mov_b32_e32 v128, v147
	v_mov_b32_e32 v129, v147
	v_mov_b32_e32 v22, v147
	v_mov_b32_e32 v23, v147
	v_mov_b32_e32 v24, v147
	v_mov_b32_e32 v25, v147
	v_mov_b32_e32 v18, v147
	v_mov_b32_e32 v19, v147
	v_mov_b32_e32 v20, v147
	v_mov_b32_e32 v21, v147
	v_mov_b32_e32 v10, v147
	v_mov_b32_e32 v11, v147
	v_mov_b32_e32 v12, v147
	v_mov_b32_e32 v13, v147
	v_mov_b32_e32 v6, v147
	v_mov_b32_e32 v7, v147
	v_mov_b32_e32 v8, v147
	v_mov_b32_e32 v9, v147
	.p2align 6
	s_nop 0
	s_nop 0
	s_nop 0
	s_nop 0
	s_nop 0
	s_nop 0
	s_nop 0
	s_nop 0

; template <class Epi, class Sched, bool ALIGN_EPI = false>
; __device__ __forceinline__ void gemm_phase(PG8_LAS unsigned char* lds, const Gemm g, const Sched& S, const Epi& E) {
;     ...
;         const char* nA = Sched::GATHER ? (const char*)g.A : (has_next ? (const char*)g.A + (size_t)nxt.pm * tstep : cA); const char* nB = has_next ? (const char*)g.Bt + nxt.boff + (size_t)nxt.pn * tstep : cB;
;         for (int t = 0; t < nt; t += 2) {
;             const bool last = (t == nt - 2);
;             const char* a1 = cA + (size_t)(t + 1) * kstep;
;             const char* a2 = last ? nA : cA + (size_t)(t + 2) * kstep; const char* b2 = last ? nB : cB + (size_t)(t + 2) * kstep;
;             const char* a3 = a2 + kstep; const char* b3 = b2 + kstep;
;             unsigned w0[2], w1[2];
; #pragma unroll
;             for (int i = 0; i < 2; ++i) { w0[i] = (Sched::GATHER && last) ? vn0[i] : vc0[i]; w1[i] = (Sched::GATHER && last) ? vn1[i] : vc1[i]; }
;             if (last && has_next) S.a_ready(nxt);
;             PG8_LDB(B0, 0, 0); PG8_LDB(B1, 0, 1); PG8_SCHED; PG8_LDA(At, 0, 0); PG8_STAGE(PG8_SA(1, 1), a1 + hstepA, vc1);
;             PG8_WAIT_V(8); PG8_WAIT_L(0); PG8_BAR; PG8_MMA(0, 0, At, B0); PG8_MMA(0, 1, At, B1); PG8_BAR; PG8_SCHED;
;             PG8_LDA(At, 0, 1); PG8_STAGE(PG8_SB(0, 0), b2, voffB); PG8_STAGE(PG8_SB(0, 1), b2 + hstep, voffB); PG8_STAGE(PG8_SA(0, 0), a2, w0);
;             PG8_WAIT_V(8); PG8_WAIT_L(0); PG8_BAR; PG8_MMA(1, 0, At, B0); PG8_MMA(1, 1, At, B1); PG8_BAR; PG8_SCHED;
;             PG8_LDB(B0, 1, 0); PG8_LDB(B1, 1, 1); PG8_SCHED; PG8_LDA(At, 1, 0); PG8_STAGE(PG8_SA(0, 1), a2 + hstepA, w1);
;             PG8_WAIT_V(8); PG8_WAIT_L(0); PG8_BAR; PG8_MMA(0, 0, At, B0); PG8_MMA(0, 1, At, B1); PG8_BAR; PG8_SCHED;
;             PG8_LDA(At, 1, 1); PG8_STAGE(PG8_SB(1, 0), b3, voffB); PG8_STAGE(PG8_SB(1, 1), b3 + hstep, voffB); PG8_STAGE(PG8_SA(1, 0), a3, w0);
;             PG8_WAIT_V(8); PG8_WAIT_L(0); PG8_BAR; PG8_MMA(1, 0, At, B0); PG8_MMA(1, 1, At, B1); PG8_BAR; PG8_SCHED;
;             if constexpr (Epi::KSCALE) { if (((t + 2) & 7) == 0 && t + 2 < nt) { E.kscale(acc, pf, ((t + 2) >> 3) - 1, wr, fr); PG8_SCHED; } }
;         }
;         if constexpr (ALIGN_EPI) { if (wr == 0) PG8_BAR; }
;         if constexpr (!Epi::AFTER_DRAIN) { E(acc, cur, wr, wc, fr, fq, pf); S.done(cur); }
;         if (!has_next) break;
; #pragma unroll
.LBB0_804:
	s_ashr_i32 s45, s44, 31
	s_lshl_b64 s[52:53], s[44:45], 18
	s_add_u32 s52, s6, s52
	s_addc_u32 s53, s7, s53
	s_and_b64 s[54:55], s[50:51], exec
	s_cselect_b32 s45, s53, s63
	s_cselect_b32 s57, s52, s62
	s_add_u32 s64, s3, s48
	s_addc_u32 s65, s35, s49
	s_ashr_i32 s47, s46, 31
	s_lshl_b64 s[54:55], s[46:47], 18
	s_add_u32 s54, s64, s54
	s_addc_u32 s55, s65, s55
	s_and_b64 s[64:65], s[50:51], exec
	s_cselect_b32 s47, s55, s61
	s_cselect_b32 s89, s54, s60
	s_add_u32 s90, s60, 0x100
	s_addc_u32 s91, s61, 0
	s_add_u32 s60, s62, 0x20080
	v_mov_b32_e32 v2, 0
	s_addc_u32 s61, s63, 0
	s_mov_b32 s92, -2
	v_mov_b32_e32 v3, v2
	v_mov_b32_e32 v4, v2
	v_mov_b32_e32 v5, v2
	v_mov_b32_e32 v6, v2
	v_mov_b32_e32 v7, v2
	v_mov_b32_e32 v8, v2
	v_mov_b32_e32 v9, v2
	v_mov_b32_e32 v10, v2
	v_mov_b32_e32 v11, v2
	v_mov_b32_e32 v12, v2
	v_mov_b32_e32 v13, v2
	v_mov_b32_e32 v14, v2
	v_mov_b32_e32 v15, v2
	v_mov_b32_e32 v16, v2
	v_mov_b32_e32 v17, v2
	v_mov_b32_e32 v26, v2
	v_mov_b32_e32 v27, v2
	v_mov_b32_e32 v28, v2
	v_mov_b32_e32 v29, v2
	v_mov_b32_e32 v30, v2
	v_mov_b32_e32 v31, v2
	v_mov_b32_e32 v32, v2
	v_mov_b32_e32 v33, v2
	v_mov_b32_e32 v42, v2
	v_mov_b32_e32 v43, v2
	v_mov_b32_e32 v44, v2
	v_mov_b32_e32 v45, v2
	v_mov_b32_e32 v54, v2
	v_mov_b32_e32 v55, v2
	v_mov_b32_e32 v56, v2
	v_mov_b32_e32 v57, v2
	v_mov_b32_e32 v58, v2
	v_mov_b32_e32 v59, v2
	v_mov_b32_e32 v60, v2
	v_mov_b32_e32 v61, v2
	v_mov_b32_e32 v62, v2
	v_mov_b32_e32 v63, v2
	v_mov_b32_e32 v64, v2
	v_mov_b32_e32 v65, v2
	v_mov_b32_e32 v78, v2
	v_mov_b32_e32 v79, v2
	v_mov_b32_e32 v80, v2
	v_mov_b32_e32 v81, v2
	v_mov_b32_e32 v86, v2
	v_mov_b32_e32 v87, v2
	v_mov_b32_e32 v88, v2
	v_mov_b32_e32 v89, v2
	v_mov_b32_e32 v94, v2
	v_mov_b32_e32 v95, v2
	v_mov_b32_e32 v96, v2
	v_mov_b32_e32 v97, v2
	v_mov_b32_e32 v102, v2
	v_mov_b32_e32 v103, v2
	v_mov_b32_e32 v104, v2
	v_mov_b32_e32 v105, v2
	v_mov_b32_e32 v110, v2
	v_mov_b32_e32 v111, v2
	v_mov_b32_e32 v112, v2
	v_mov_b32_e32 v113, v2
	v_mov_b32_e32 v118, v2
	v_mov_b32_e32 v119, v2
	v_mov_b32_e32 v120, v2
	v_mov_b32_e32 v121, v2
	v_mov_b32_e32 v74, v2
	v_mov_b32_e32 v75, v2
	v_mov_b32_e32 v76, v2
	v_mov_b32_e32 v77, v2
	v_mov_b32_e32 v82, v2
	v_mov_b32_e32 v83, v2
	v_mov_b32_e32 v84, v2
	v_mov_b32_e32 v85, v2
	v_mov_b32_e32 v90, v2
	v_mov_b32_e32 v91, v2
	v_mov_b32_e32 v92, v2
	v_mov_b32_e32 v93, v2
	v_mov_b32_e32 v98, v2
	v_mov_b32_e32 v99, v2
	v_mov_b32_e32 v100, v2
	v_mov_b32_e32 v101, v2
	v_mov_b32_e32 v106, v2
	v_mov_b32_e32 v107, v2
	v_mov_b32_e32 v108, v2
	v_mov_b32_e32 v109, v2
	v_mov_b32_e32 v114, v2
	v_mov_b32_e32 v115, v2
	v_mov_b32_e32 v116, v2
	v_mov_b32_e32 v117, v2
	v_mov_b32_e32 v122, v2
	v_mov_b32_e32 v123, v2
	v_mov_b32_e32 v124, v2
	v_mov_b32_e32 v125, v2
	v_mov_b32_e32 v126, v2
	v_mov_b32_e32 v127, v2
	v_mov_b32_e32 v128, v2
	v_mov_b32_e32 v129, v2
	v_mov_b32_e32 v70, v2
	v_mov_b32_e32 v71, v2
	v_mov_b32_e32 v72, v2
	v_mov_b32_e32 v73, v2
	v_mov_b32_e32 v66, v2
	v_mov_b32_e32 v67, v2
	v_mov_b32_e32 v68, v2
	v_mov_b32_e32 v69, v2
	v_mov_b32_e32 v50, v2
	v_mov_b32_e32 v51, v2
	v_mov_b32_e32 v52, v2
	v_mov_b32_e32 v53, v2
	v_mov_b32_e32 v46, v2
	v_mov_b32_e32 v47, v2
	v_mov_b32_e32 v48, v2
	v_mov_b32_e32 v49, v2
	v_mov_b32_e32 v38, v2
	v_mov_b32_e32 v39, v2
	v_mov_b32_e32 v40, v2
	v_mov_b32_e32 v41, v2
	v_mov_b32_e32 v34, v2
	v_mov_b32_e32 v35, v2
	v_mov_b32_e32 v36, v2
	v_mov_b32_e32 v37, v2
	v_mov_b32_e32 v22, v2
	v_mov_b32_e32 v23, v2
	v_mov_b32_e32 v24, v2
	v_mov_b32_e32 v25, v2
	v_mov_b32_e32 v18, v2
	v_mov_b32_e32 v19, v2
	v_mov_b32_e32 v20, v2
	v_mov_b32_e32 v21, v2
	.p2align 6
	s_nop 0
	s_nop 0
	s_nop 0
	s_nop 0
	s_nop 0
	s_nop 0
	s_nop 0
	s_nop 0

; template <class Epi, class Sched, bool ALIGN_EPI = false>
; __device__ __forceinline__ void gemm_phase(PG8_LAS unsigned char* lds, const Gemm g, const Sched& S, const Epi& E) {
;     ...
;         const char* nA = Sched::GATHER ? (const char*)g.A : (has_next ? (const char*)g.A + (size_t)nxt.pm * tstep : cA); const char* nB = has_next ? (const char*)g.Bt + nxt.boff + (size_t)nxt.pn * tstep : cB;
;         for (int t = 0; t < nt; t += 2) {
;             const bool last = (t == nt - 2);
;             const char* a1 = cA + (size_t)(t + 1) * kstep;
;             const char* a2 = last ? nA : cA + (size_t)(t + 2) * kstep; const char* b2 = last ? nB : cB + (size_t)(t + 2) * kstep;
;             const char* a3 = a2 + kstep; const char* b3 = b2 + kstep;
;             unsigned w0[2], w1[2];
; #pragma unroll
;             for (int i = 0; i < 2; ++i) { w0[i] = (Sched::GATHER && last) ? vn0[i] : vc0[i]; w1[i] = (Sched::GATHER && last) ? vn1[i] : vc1[i]; }
;             if (last && has_next) S.a_ready(nxt);
;             PG8_LDB(B0, 0, 0); PG8_LDB(B1, 0, 1); PG8_SCHED; PG8_LDA(At, 0, 0); PG8_STAGE(PG8_SA(1, 1), a1 + hstepA, vc1);
;             PG8_WAIT_V(8); PG8_WAIT_L(0); PG8_BAR; PG8_MMA(0, 0, At, B0); PG8_MMA(0, 1, At, B1); PG8_BAR; PG8_SCHED;
;             PG8_LDA(At, 0, 1); PG8_STAGE(PG8_SB(0, 0), b2, voffB); PG8_STAGE(PG8_SB(0, 1), b2 + hstep, voffB); PG8_STAGE(PG8_SA(0, 0), a2, w0);
;             PG8_WAIT_V(8); PG8_WAIT_L(0); PG8_BAR; PG8_MMA(1, 0, At, B0); PG8_MMA(1, 1, At, B1); PG8_BAR; PG8_SCHED;
;             PG8_LDB(B0, 1, 0); PG8_LDB(B1, 1, 1); PG8_SCHED; PG8_LDA(At, 1, 0); PG8_STAGE(PG8_SA(0, 1), a2 + hstepA, w1);
;             PG8_WAIT_V(8); PG8_WAIT_L(0); PG8_BAR; PG8_MMA(0, 0, At, B0); PG8_MMA(0, 1, At, B1); PG8_BAR; PG8_SCHED;
;             PG8_LDA(At, 1, 1); PG8_STAGE(PG8_SB(1, 0), b3, voffB); PG8_STAGE(PG8_SB(1, 1), b3 + hstep, voffB); PG8_STAGE(PG8_SA(1, 0), a3, w0);
;             PG8_WAIT_V(8); PG8_WAIT_L(0); PG8_BAR; PG8_MMA(1, 0, At, B0); PG8_MMA(1, 1, At, B1); PG8_BAR; PG8_SCHED;
;             if constexpr (Epi::KSCALE) { if (((t + 2) & 7) == 0 && t + 2 < nt) { E.kscale(acc, pf, ((t + 2) >> 3) - 1, wr, fr); PG8_SCHED; } }
;         }
;         if constexpr (ALIGN_EPI) { if (wr == 0) PG8_BAR; }
;         if constexpr (!Epi::AFTER_DRAIN) { E(acc, cur, wr, wc, fr, fq, pf); S.done(cur); }
;         if (!has_next) break;
; #pragma unroll
.LBB0_907:
	s_ashr_i32 s41, s40, 31
	s_lshl_b64 s[50:51], s[40:41], 18
	s_add_u32 s50, s62, s50
	s_addc_u32 s51, s63, s51
	s_and_b64 s[54:55], s[52:53], exec
	s_cselect_b32 s41, s51, s59
	s_cselect_b32 s47, s50, s58
	s_add_u32 s60, s64, s44
	s_addc_u32 s61, s65, s45
	s_ashr_i32 s43, s42, 31
	s_lshl_b64 s[54:55], s[42:43], 18
	s_add_u32 s54, s60, s54
	s_addc_u32 s55, s61, s55
	s_and_b64 s[60:61], s[52:53], exec
	s_cselect_b32 s43, s55, s57
	s_cselect_b32 s89, s54, s56
	s_add_u32 s90, s56, 0x100
	s_addc_u32 s91, s57, 0
	s_add_u32 s56, s58, 0x20080
	v_mov_b32_e32 v2, 0
	s_addc_u32 s57, s59, 0
	s_mov_b32 s92, -2
	v_mov_b32_e32 v3, v2
	v_mov_b32_e32 v4, v2
	v_mov_b32_e32 v5, v2
	v_mov_b32_e32 v6, v2
	v_mov_b32_e32 v7, v2
	v_mov_b32_e32 v8, v2
	v_mov_b32_e32 v9, v2
	v_mov_b32_e32 v10, v2
	v_mov_b32_e32 v11, v2
	v_mov_b32_e32 v12, v2
	v_mov_b32_e32 v13, v2
	v_mov_b32_e32 v14, v2
	v_mov_b32_e32 v15, v2
	v_mov_b32_e32 v16, v2
	v_mov_b32_e32 v17, v2
	v_mov_b32_e32 v26, v2
	v_mov_b32_e32 v27, v2
	v_mov_b32_e32 v28, v2
	v_mov_b32_e32 v29, v2
	v_mov_b32_e32 v30, v2
	v_mov_b32_e32 v31, v2
	v_mov_b32_e32 v32, v2
	v_mov_b32_e32 v33, v2
	v_mov_b32_e32 v42, v2
	v_mov_b32_e32 v43, v2
	v_mov_b32_e32 v44, v2
	v_mov_b32_e32 v45, v2
	v_mov_b32_e32 v54, v2
	v_mov_b32_e32 v55, v2
	v_mov_b32_e32 v56, v2
	v_mov_b32_e32 v57, v2
	v_mov_b32_e32 v58, v2
	v_mov_b32_e32 v59, v2
	v_mov_b32_e32 v60, v2
	v_mov_b32_e32 v61, v2
	v_mov_b32_e32 v62, v2
	v_mov_b32_e32 v63, v2
	v_mov_b32_e32 v64, v2
	v_mov_b32_e32 v65, v2
	v_mov_b32_e32 v78, v2
	v_mov_b32_e32 v79, v2
	v_mov_b32_e32 v80, v2
	v_mov_b32_e32 v81, v2
	v_mov_b32_e32 v86, v2
	v_mov_b32_e32 v87, v2
	v_mov_b32_e32 v88, v2
	v_mov_b32_e32 v89, v2
	v_mov_b32_e32 v94, v2
	v_mov_b32_e32 v95, v2
	v_mov_b32_e32 v96, v2
	v_mov_b32_e32 v97, v2
	v_mov_b32_e32 v102, v2
	v_mov_b32_e32 v103, v2
	v_mov_b32_e32 v104, v2
	v_mov_b32_e32 v105, v2
	v_mov_b32_e32 v110, v2
	v_mov_b32_e32 v111, v2
	v_mov_b32_e32 v112, v2
	v_mov_b32_e32 v113, v2
	v_mov_b32_e32 v118, v2
	v_mov_b32_e32 v119, v2
	v_mov_b32_e32 v120, v2
	v_mov_b32_e32 v121, v2
	v_mov_b32_e32 v74, v2
	v_mov_b32_e32 v75, v2
	v_mov_b32_e32 v76, v2
	v_mov_b32_e32 v77, v2
	v_mov_b32_e32 v82, v2
	v_mov_b32_e32 v83, v2
	v_mov_b32_e32 v84, v2
	v_mov_b32_e32 v85, v2
	v_mov_b32_e32 v90, v2
	v_mov_b32_e32 v91, v2
	v_mov_b32_e32 v92, v2
	v_mov_b32_e32 v93, v2
	v_mov_b32_e32 v98, v2
	v_mov_b32_e32 v99, v2
	v_mov_b32_e32 v100, v2
	v_mov_b32_e32 v101, v2
	v_mov_b32_e32 v106, v2
	v_mov_b32_e32 v107, v2
	v_mov_b32_e32 v108, v2
	v_mov_b32_e32 v109, v2
	v_mov_b32_e32 v114, v2
	v_mov_b32_e32 v115, v2
	v_mov_b32_e32 v116, v2
	v_mov_b32_e32 v117, v2
	v_mov_b32_e32 v122, v2
	v_mov_b32_e32 v123, v2
	v_mov_b32_e32 v124, v2
	v_mov_b32_e32 v125, v2
	v_mov_b32_e32 v126, v2
	v_mov_b32_e32 v127, v2
	v_mov_b32_e32 v128, v2
	v_mov_b32_e32 v129, v2
	v_mov_b32_e32 v70, v2
	v_mov_b32_e32 v71, v2
	v_mov_b32_e32 v72, v2
	v_mov_b32_e32 v73, v2
	v_mov_b32_e32 v66, v2
	v_mov_b32_e32 v67, v2
	v_mov_b32_e32 v68, v2
	v_mov_b32_e32 v69, v2
	v_mov_b32_e32 v50, v2
	v_mov_b32_e32 v51, v2
	v_mov_b32_e32 v52, v2
	v_mov_b32_e32 v53, v2
	v_mov_b32_e32 v46, v2
	v_mov_b32_e32 v47, v2
	v_mov_b32_e32 v48, v2
	v_mov_b32_e32 v49, v2
	v_mov_b32_e32 v38, v2
	v_mov_b32_e32 v39, v2
	v_mov_b32_e32 v40, v2
	v_mov_b32_e32 v41, v2
	v_mov_b32_e32 v34, v2
	v_mov_b32_e32 v35, v2
	v_mov_b32_e32 v36, v2
	v_mov_b32_e32 v37, v2
	v_mov_b32_e32 v22, v2
	v_mov_b32_e32 v23, v2
	v_mov_b32_e32 v24, v2
	v_mov_b32_e32 v25, v2
	v_mov_b32_e32 v18, v2
	v_mov_b32_e32 v19, v2
	v_mov_b32_e32 v20, v2
	v_mov_b32_e32 v21, v2
	.p2align 6
	s_nop 0
	s_nop 0
	s_nop 0
	s_nop 0
	s_nop 0
	s_nop 0
	s_nop 0
	s_nop 0

; template <class Epi, class Sched, bool ALIGN_EPI = false>
; __device__ __forceinline__ void gemm_phase(PG8_LAS unsigned char* lds, const Gemm g, const Sched& S, const Epi& E) {
;     ...
;         const char* nA = Sched::GATHER ? (const char*)g.A : (has_next ? (const char*)g.A + (size_t)nxt.pm * tstep : cA); const char* nB = has_next ? (const char*)g.Bt + nxt.boff + (size_t)nxt.pn * tstep : cB;
;         for (int t = 0; t < nt; t += 2) {
;             const bool last = (t == nt - 2);
;             const char* a1 = cA + (size_t)(t + 1) * kstep;
;             const char* a2 = last ? nA : cA + (size_t)(t + 2) * kstep; const char* b2 = last ? nB : cB + (size_t)(t + 2) * kstep;
;             const char* a3 = a2 + kstep; const char* b3 = b2 + kstep;
;             unsigned w0[2], w1[2];
; #pragma unroll
;             for (int i = 0; i < 2; ++i) { w0[i] = (Sched::GATHER && last) ? vn0[i] : vc0[i]; w1[i] = (Sched::GATHER && last) ? vn1[i] : vc1[i]; }
;             if (last && has_next) S.a_ready(nxt);
;             PG8_LDB(B0, 0, 0); PG8_LDB(B1, 0, 1); PG8_SCHED; PG8_LDA(At, 0, 0); PG8_STAGE(PG8_SA(1, 1), a1 + hstepA, vc1);
;             PG8_WAIT_V(8); PG8_WAIT_L(0); PG8_BAR; PG8_MMA(0, 0, At, B0); PG8_MMA(0, 1, At, B1); PG8_BAR; PG8_SCHED;
;             PG8_LDA(At, 0, 1); PG8_STAGE(PG8_SB(0, 0), b2, voffB); PG8_STAGE(PG8_SB(0, 1), b2 + hstep, voffB); PG8_STAGE(PG8_SA(0, 0), a2, w0);
;             PG8_WAIT_V(8); PG8_WAIT_L(0); PG8_BAR; PG8_MMA(1, 0, At, B0); PG8_MMA(1, 1, At, B1); PG8_BAR; PG8_SCHED;
;             PG8_LDB(B0, 1, 0); PG8_LDB(B1, 1, 1); PG8_SCHED; PG8_LDA(At, 1, 0); PG8_STAGE(PG8_SA(0, 1), a2 + hstepA, w1);
;             PG8_WAIT_V(8); PG8_WAIT_L(0); PG8_BAR; PG8_MMA(0, 0, At, B0); PG8_MMA(0, 1, At, B1); PG8_BAR; PG8_SCHED;
;             PG8_LDA(At, 1, 1); PG8_STAGE(PG8_SB(1, 0), b3, voffB); PG8_STAGE(PG8_SB(1, 1), b3 + hstep, voffB); PG8_STAGE(PG8_SA(1, 0), a3, w0);
;             PG8_WAIT_V(8); PG8_WAIT_L(0); PG8_BAR; PG8_MMA(1, 0, At, B0); PG8_MMA(1, 1, At, B1); PG8_BAR; PG8_SCHED;
;             if constexpr (Epi::KSCALE) { if (((t + 2) & 7) == 0 && t + 2 < nt) { E.kscale(acc, pf, ((t + 2) >> 3) - 1, wr, fr); PG8_SCHED; } }
;         }
;         if constexpr (ALIGN_EPI) { if (wr == 0) PG8_BAR; }
;         if constexpr (!Epi::AFTER_DRAIN) { E(acc, cur, wr, wc, fr, fq, pf); S.done(cur); }
;         if (!has_next) break;
; #pragma unroll
.LBB0_1054:
	s_ashr_i32 s15, s14, 31
	s_lshl_b64 s[50:51], s[14:15], 20
	s_add_u32 s50, s12, s50
	s_addc_u32 s51, s13, s51
	s_and_b64 s[52:53], s[10:11], exec
	s_cselect_b32 s15, s51, s55
	s_cselect_b32 s79, s50, s54
	s_ashr_i32 s49, s48, 31
	s_lshl_b64 s[52:53], s[48:49], 20
	s_add_u32 s52, s3, s52
	s_addc_u32 s53, s35, s53
	s_and_b64 s[58:59], s[10:11], exec
	s_cselect_b32 s49, s53, s57
	s_cselect_b32 s80, s52, s56
	s_add_u32 s54, s54, 0x80080
	s_addc_u32 s55, s55, 0
	s_add_u32 s81, s56, 0x100
	v_mov_b32_e32 v2, 0
	s_addc_u32 s82, s57, 0
	s_mov_b32 s83, -2
	v_mov_b32_e32 v3, v2
	v_mov_b32_e32 v4, v2
	v_mov_b32_e32 v5, v2
	v_mov_b32_e32 v6, v2
	v_mov_b32_e32 v7, v2
	v_mov_b32_e32 v8, v2
	v_mov_b32_e32 v9, v2
	v_mov_b32_e32 v10, v2
	v_mov_b32_e32 v11, v2
	v_mov_b32_e32 v12, v2
	v_mov_b32_e32 v13, v2
	v_mov_b32_e32 v14, v2
	v_mov_b32_e32 v15, v2
	v_mov_b32_e32 v16, v2
	v_mov_b32_e32 v17, v2
	v_mov_b32_e32 v26, v2
	v_mov_b32_e32 v27, v2
	v_mov_b32_e32 v28, v2
	v_mov_b32_e32 v29, v2
	v_mov_b32_e32 v30, v2
	v_mov_b32_e32 v31, v2
	v_mov_b32_e32 v32, v2
	v_mov_b32_e32 v33, v2
	v_mov_b32_e32 v42, v2
	v_mov_b32_e32 v43, v2
	v_mov_b32_e32 v44, v2
	v_mov_b32_e32 v45, v2
	v_mov_b32_e32 v54, v2
	v_mov_b32_e32 v55, v2
	v_mov_b32_e32 v56, v2
	v_mov_b32_e32 v57, v2
	v_mov_b32_e32 v58, v2
	v_mov_b32_e32 v59, v2
	v_mov_b32_e32 v60, v2
	v_mov_b32_e32 v61, v2
	v_mov_b32_e32 v62, v2
	v_mov_b32_e32 v63, v2
	v_mov_b32_e32 v64, v2
	v_mov_b32_e32 v65, v2
	v_mov_b32_e32 v78, v2
	v_mov_b32_e32 v79, v2
	v_mov_b32_e32 v80, v2
	v_mov_b32_e32 v81, v2
	v_mov_b32_e32 v86, v2
	v_mov_b32_e32 v87, v2
	v_mov_b32_e32 v88, v2
	v_mov_b32_e32 v89, v2
	v_mov_b32_e32 v94, v2
	v_mov_b32_e32 v95, v2
	v_mov_b32_e32 v96, v2
	v_mov_b32_e32 v97, v2
	v_mov_b32_e32 v102, v2
	v_mov_b32_e32 v103, v2
	v_mov_b32_e32 v104, v2
	v_mov_b32_e32 v105, v2
	v_mov_b32_e32 v110, v2
	v_mov_b32_e32 v111, v2
	v_mov_b32_e32 v112, v2
	v_mov_b32_e32 v113, v2
	v_mov_b32_e32 v118, v2
	v_mov_b32_e32 v119, v2
	v_mov_b32_e32 v120, v2
	v_mov_b32_e32 v121, v2
	v_mov_b32_e32 v74, v2
	v_mov_b32_e32 v75, v2
	v_mov_b32_e32 v76, v2
	v_mov_b32_e32 v77, v2
	v_mov_b32_e32 v82, v2
	v_mov_b32_e32 v83, v2
	v_mov_b32_e32 v84, v2
	v_mov_b32_e32 v85, v2
	v_mov_b32_e32 v90, v2
	v_mov_b32_e32 v91, v2
	v_mov_b32_e32 v92, v2
	v_mov_b32_e32 v93, v2
	v_mov_b32_e32 v98, v2
	v_mov_b32_e32 v99, v2
	v_mov_b32_e32 v100, v2
	v_mov_b32_e32 v101, v2
	v_mov_b32_e32 v106, v2
	v_mov_b32_e32 v107, v2
	v_mov_b32_e32 v108, v2
	v_mov_b32_e32 v109, v2
	v_mov_b32_e32 v114, v2
	v_mov_b32_e32 v115, v2
	v_mov_b32_e32 v116, v2
	v_mov_b32_e32 v117, v2
	v_mov_b32_e32 v122, v2
	v_mov_b32_e32 v123, v2
	v_mov_b32_e32 v124, v2
	v_mov_b32_e32 v125, v2
	v_mov_b32_e32 v126, v2
	v_mov_b32_e32 v127, v2
	v_mov_b32_e32 v128, v2
	v_mov_b32_e32 v129, v2
	v_mov_b32_e32 v66, v2
	v_mov_b32_e32 v67, v2
	v_mov_b32_e32 v68, v2
	v_mov_b32_e32 v69, v2
	v_mov_b32_e32 v70, v2
	v_mov_b32_e32 v71, v2
	v_mov_b32_e32 v72, v2
	v_mov_b32_e32 v73, v2
	v_mov_b32_e32 v46, v2
	v_mov_b32_e32 v47, v2
	v_mov_b32_e32 v48, v2
	v_mov_b32_e32 v49, v2
	v_mov_b32_e32 v50, v2
	v_mov_b32_e32 v51, v2
	v_mov_b32_e32 v52, v2
	v_mov_b32_e32 v53, v2
	v_mov_b32_e32 v34, v2
	v_mov_b32_e32 v35, v2
	v_mov_b32_e32 v36, v2
	v_mov_b32_e32 v37, v2
	v_mov_b32_e32 v38, v2
	v_mov_b32_e32 v39, v2
	v_mov_b32_e32 v40, v2
	v_mov_b32_e32 v41, v2
	v_mov_b32_e32 v18, v2
	v_mov_b32_e32 v19, v2
	v_mov_b32_e32 v20, v2
	v_mov_b32_e32 v21, v2
	v_mov_b32_e32 v22, v2
	v_mov_b32_e32 v23, v2
	v_mov_b32_e32 v24, v2
	v_mov_b32_e32 v25, v2
	.p2align 6
	s_nop 0
	s_nop 0
	s_nop 0
	s_nop 0
	s_nop 0
	s_nop 0
	s_nop 0
	s_nop 0

; template <class Epi, class Sched, bool ALIGN_EPI = false>
; __device__ __forceinline__ void gemm_phase(PG8_LAS unsigned char* lds, const Gemm g, const Sched& S, const Epi& E) {
;     ...
;         const char* nA = Sched::GATHER ? (const char*)g.A : (has_next ? (const char*)g.A + (size_t)nxt.pm * tstep : cA); const char* nB = has_next ? (const char*)g.Bt + nxt.boff + (size_t)nxt.pn * tstep : cB;
;         for (int t = 0; t < nt; t += 2) {
;             const bool last = (t == nt - 2);
;             const char* a1 = cA + (size_t)(t + 1) * kstep;
;             const char* a2 = last ? nA : cA + (size_t)(t + 2) * kstep; const char* b2 = last ? nB : cB + (size_t)(t + 2) * kstep;
;             const char* a3 = a2 + kstep; const char* b3 = b2 + kstep;
;             unsigned w0[2], w1[2];
; #pragma unroll
;             for (int i = 0; i < 2; ++i) { w0[i] = (Sched::GATHER && last) ? vn0[i] : vc0[i]; w1[i] = (Sched::GATHER && last) ? vn1[i] : vc1[i]; }
;             if (last && has_next) S.a_ready(nxt);
;             PG8_LDB(B0, 0, 0); PG8_LDB(B1, 0, 1); PG8_SCHED; PG8_LDA(At, 0, 0); PG8_STAGE(PG8_SA(1, 1), a1 + hstepA, vc1);
;             PG8_WAIT_V(8); PG8_WAIT_L(0); PG8_BAR; PG8_MMA(0, 0, At, B0); PG8_MMA(0, 1, At, B1); PG8_BAR; PG8_SCHED;
;             PG8_LDA(At, 0, 1); PG8_STAGE(PG8_SB(0, 0), b2, voffB); PG8_STAGE(PG8_SB(0, 1), b2 + hstep, voffB); PG8_STAGE(PG8_SA(0, 0), a2, w0);
;             PG8_WAIT_V(8); PG8_WAIT_L(0); PG8_BAR; PG8_MMA(1, 0, At, B0); PG8_MMA(1, 1, At, B1); PG8_BAR; PG8_SCHED;
;             PG8_LDB(B0, 1, 0); PG8_LDB(B1, 1, 1); PG8_SCHED; PG8_LDA(At, 1, 0); PG8_STAGE(PG8_SA(0, 1), a2 + hstepA, w1);
;             PG8_WAIT_V(8); PG8_WAIT_L(0); PG8_BAR; PG8_MMA(0, 0, At, B0); PG8_MMA(0, 1, At, B1); PG8_BAR; PG8_SCHED;
;             PG8_LDA(At, 1, 1); PG8_STAGE(PG8_SB(1, 0), b3, voffB); PG8_STAGE(PG8_SB(1, 1), b3 + hstep, voffB); PG8_STAGE(PG8_SA(1, 0), a3, w0);
;             PG8_WAIT_V(8); PG8_WAIT_L(0); PG8_BAR; PG8_MMA(1, 0, At, B0); PG8_MMA(1, 1, At, B1); PG8_BAR; PG8_SCHED;
;             if constexpr (Epi::KSCALE) { if (((t + 2) & 7) == 0 && t + 2 < nt) { E.kscale(acc, pf, ((t + 2) >> 3) - 1, wr, fr); PG8_SCHED; } }
;         }
;         if constexpr (ALIGN_EPI) { if (wr == 0) PG8_BAR; }
;         if constexpr (!Epi::AFTER_DRAIN) { E(acc, cur, wr, wc, fr, fq, pf); S.done(cur); }
;         if (!has_next) break;
; #pragma unroll
.LBB0_1197:
	s_ashr_i32 s45, s44, 31
	s_lshl_b64 s[46:47], s[44:45], 20
	s_add_u32 s46, s3, s46
	s_addc_u32 s47, s35, s47
	s_and_b64 s[48:49], s[10:11], exec
	s_cselect_b32 s45, s47, s53
	s_cselect_b32 s74, s46, s52
	s_ashr_i32 s43, s42, 31
	s_lshl_b64 s[48:49], s[42:43], 20
	s_add_u32 s48, s58, s48
	s_addc_u32 s49, s59, s49
	s_and_b64 s[56:57], s[10:11], exec
	s_cselect_b32 s43, s49, s55
	s_cselect_b32 s75, s48, s54
	s_add_u32 s52, s52, 0x80080
	s_addc_u32 s53, s53, 0
	s_add_u32 s76, s54, 0x100
	v_mov_b32_e32 v2, 0
	s_addc_u32 s77, s55, 0
	s_mov_b32 s78, -2
	v_mov_b32_e32 v3, v2
	v_mov_b32_e32 v4, v2
	v_mov_b32_e32 v5, v2
	v_mov_b32_e32 v6, v2
	v_mov_b32_e32 v7, v2
	v_mov_b32_e32 v8, v2
	v_mov_b32_e32 v9, v2
	v_mov_b32_e32 v18, v2
	v_mov_b32_e32 v19, v2
	v_mov_b32_e32 v20, v2
	v_mov_b32_e32 v21, v2
	v_mov_b32_e32 v22, v2
	v_mov_b32_e32 v23, v2
	v_mov_b32_e32 v24, v2
	v_mov_b32_e32 v25, v2
	v_mov_b32_e32 v34, v2
	v_mov_b32_e32 v35, v2
	v_mov_b32_e32 v36, v2
	v_mov_b32_e32 v37, v2
	v_mov_b32_e32 v38, v2
	v_mov_b32_e32 v39, v2
	v_mov_b32_e32 v40, v2
	v_mov_b32_e32 v41, v2
	v_mov_b32_e32 v50, v2
	v_mov_b32_e32 v51, v2
	v_mov_b32_e32 v52, v2
	v_mov_b32_e32 v53, v2
	v_mov_b32_e32 v54, v2
	v_mov_b32_e32 v55, v2
	v_mov_b32_e32 v56, v2
	v_mov_b32_e32 v57, v2
	v_mov_b32_e32 v66, v2
	v_mov_b32_e32 v67, v2
	v_mov_b32_e32 v68, v2
	v_mov_b32_e32 v69, v2
	v_mov_b32_e32 v70, v2
	v_mov_b32_e32 v71, v2
	v_mov_b32_e32 v72, v2
	v_mov_b32_e32 v73, v2
	v_mov_b32_e32 v82, v2
	v_mov_b32_e32 v83, v2
	v_mov_b32_e32 v84, v2
	v_mov_b32_e32 v85, v2
	v_mov_b32_e32 v86, v2
	v_mov_b32_e32 v87, v2
	v_mov_b32_e32 v88, v2
	v_mov_b32_e32 v89, v2
	v_mov_b32_e32 v98, v2
	v_mov_b32_e32 v99, v2
	v_mov_b32_e32 v100, v2
	v_mov_b32_e32 v101, v2
	v_mov_b32_e32 v102, v2
	v_mov_b32_e32 v103, v2
	v_mov_b32_e32 v104, v2
	v_mov_b32_e32 v105, v2
	v_mov_b32_e32 v106, v2
	v_mov_b32_e32 v107, v2
	v_mov_b32_e32 v108, v2
	v_mov_b32_e32 v109, v2
	v_mov_b32_e32 v110, v2
	v_mov_b32_e32 v111, v2
	v_mov_b32_e32 v112, v2
	v_mov_b32_e32 v113, v2
	v_mov_b32_e32 v74, v2
	v_mov_b32_e32 v75, v2
	v_mov_b32_e32 v76, v2
	v_mov_b32_e32 v77, v2
	v_mov_b32_e32 v78, v2
	v_mov_b32_e32 v79, v2
	v_mov_b32_e32 v80, v2
	v_mov_b32_e32 v81, v2
	v_mov_b32_e32 v90, v2
	v_mov_b32_e32 v91, v2
	v_mov_b32_e32 v92, v2
	v_mov_b32_e32 v93, v2
	v_mov_b32_e32 v94, v2
	v_mov_b32_e32 v95, v2
	v_mov_b32_e32 v96, v2
	v_mov_b32_e32 v97, v2
	v_mov_b32_e32 v114, v2
	v_mov_b32_e32 v115, v2
	v_mov_b32_e32 v116, v2
	v_mov_b32_e32 v117, v2
	v_mov_b32_e32 v118, v2
	v_mov_b32_e32 v119, v2
	v_mov_b32_e32 v120, v2
	v_mov_b32_e32 v121, v2
	v_mov_b32_e32 v122, v2
	v_mov_b32_e32 v123, v2
	v_mov_b32_e32 v124, v2
	v_mov_b32_e32 v125, v2
	v_mov_b32_e32 v126, v2
	v_mov_b32_e32 v127, v2
	v_mov_b32_e32 v128, v2
	v_mov_b32_e32 v129, v2
	v_mov_b32_e32 v62, v2
	v_mov_b32_e32 v63, v2
	v_mov_b32_e32 v64, v2
	v_mov_b32_e32 v65, v2
	v_mov_b32_e32 v58, v2
	v_mov_b32_e32 v59, v2
	v_mov_b32_e32 v60, v2
	v_mov_b32_e32 v61, v2
	v_mov_b32_e32 v46, v2
	v_mov_b32_e32 v47, v2
	v_mov_b32_e32 v48, v2
	v_mov_b32_e32 v49, v2
	v_mov_b32_e32 v42, v2
	v_mov_b32_e32 v43, v2
	v_mov_b32_e32 v44, v2
	v_mov_b32_e32 v45, v2
	v_mov_b32_e32 v30, v2
	v_mov_b32_e32 v31, v2
	v_mov_b32_e32 v32, v2
	v_mov_b32_e32 v33, v2
	v_mov_b32_e32 v26, v2
	v_mov_b32_e32 v27, v2
	v_mov_b32_e32 v28, v2
	v_mov_b32_e32 v29, v2
	v_mov_b32_e32 v14, v2
	v_mov_b32_e32 v15, v2
	v_mov_b32_e32 v16, v2
	v_mov_b32_e32 v17, v2
	v_mov_b32_e32 v10, v2
	v_mov_b32_e32 v11, v2
	v_mov_b32_e32 v12, v2
	v_mov_b32_e32 v13, v2
	.p2align 6
	s_nop 0
	s_nop 0
	s_nop 0
	s_nop 0
	s_nop 0
	s_nop 0
	s_nop 0
	s_nop 0

; template <class Epi, class Sched, bool ALIGN_EPI = false>
; __device__ __forceinline__ void gemm_phase(PG8_LAS unsigned char* lds, const Gemm g, const Sched& S, const Epi& E) {
;     ...
;         const char* nA = Sched::GATHER ? (const char*)g.A : (has_next ? (const char*)g.A + (size_t)nxt.pm * tstep : cA); const char* nB = has_next ? (const char*)g.Bt + nxt.boff + (size_t)nxt.pn * tstep : cB;
;         for (int t = 0; t < nt; t += 2) {
;             const bool last = (t == nt - 2);
;             const char* a1 = cA + (size_t)(t + 1) * kstep;
;             const char* a2 = last ? nA : cA + (size_t)(t + 2) * kstep; const char* b2 = last ? nB : cB + (size_t)(t + 2) * kstep;
;             const char* a3 = a2 + kstep; const char* b3 = b2 + kstep;
;             unsigned w0[2], w1[2];
; #pragma unroll
;             for (int i = 0; i < 2; ++i) { w0[i] = (Sched::GATHER && last) ? vn0[i] : vc0[i]; w1[i] = (Sched::GATHER && last) ? vn1[i] : vc1[i]; }
;             if (last && has_next) S.a_ready(nxt);
;             PG8_LDB(B0, 0, 0); PG8_LDB(B1, 0, 1); PG8_SCHED; PG8_LDA(At, 0, 0); PG8_STAGE(PG8_SA(1, 1), a1 + hstepA, vc1);
;             PG8_WAIT_V(8); PG8_WAIT_L(0); PG8_BAR; PG8_MMA(0, 0, At, B0); PG8_MMA(0, 1, At, B1); PG8_BAR; PG8_SCHED;
;             PG8_LDA(At, 0, 1); PG8_STAGE(PG8_SB(0, 0), b2, voffB); PG8_STAGE(PG8_SB(0, 1), b2 + hstep, voffB); PG8_STAGE(PG8_SA(0, 0), a2, w0);
;             PG8_WAIT_V(8); PG8_WAIT_L(0); PG8_BAR; PG8_MMA(1, 0, At, B0); PG8_MMA(1, 1, At, B1); PG8_BAR; PG8_SCHED;
;             PG8_LDB(B0, 1, 0); PG8_LDB(B1, 1, 1); PG8_SCHED; PG8_LDA(At, 1, 0); PG8_STAGE(PG8_SA(0, 1), a2 + hstepA, w1);
;             PG8_WAIT_V(8); PG8_WAIT_L(0); PG8_BAR; PG8_MMA(0, 0, At, B0); PG8_MMA(0, 1, At, B1); PG8_BAR; PG8_SCHED;
;             PG8_LDA(At, 1, 1); PG8_STAGE(PG8_SB(1, 0), b3, voffB); PG8_STAGE(PG8_SB(1, 1), b3 + hstep, voffB); PG8_STAGE(PG8_SA(1, 0), a3, w0);
;             PG8_WAIT_V(8); PG8_WAIT_L(0); PG8_BAR; PG8_MMA(1, 0, At, B0); PG8_MMA(1, 1, At, B1); PG8_BAR; PG8_SCHED;
;             if constexpr (Epi::KSCALE) { if (((t + 2) & 7) == 0 && t + 2 < nt) { E.kscale(acc, pf, ((t + 2) >> 3) - 1, wr, fr); PG8_SCHED; } }
;         }
;         if constexpr (ALIGN_EPI) { if (wr == 0) PG8_BAR; }
;         if constexpr (!Epi::AFTER_DRAIN) { E(acc, cur, wr, wc, fr, fq, pf); S.done(cur); }
;         if (!has_next) break;
; #pragma unroll
.LBB0_1413:
	v_mov_b32_e32 v153, v135
	v_mov_b32_e32 v155, v135
	s_add_u32 s47, s54, 0x100
	v_mov_b32_e32 v26, 0
	s_addc_u32 s86, s55, 0
	v_lshl_add_u64 v[158:159], s[26:27], 0, v[154:155]
	v_lshl_add_u64 v[160:161], s[26:27], 0, v[152:153]
	s_mov_b32 s87, -2
	s_mov_b64 s[54:55], 0
	v_mov_b32_e32 v27, v26
	v_mov_b32_e32 v28, v26
	v_mov_b32_e32 v29, v26
	v_mov_b32_e32 v38, v26
	v_mov_b32_e32 v39, v26
	v_mov_b32_e32 v40, v26
	v_mov_b32_e32 v41, v26
	v_mov_b32_e32 v46, v26
	v_mov_b32_e32 v47, v26
	v_mov_b32_e32 v48, v26
	v_mov_b32_e32 v49, v26
	v_mov_b32_e32 v54, v26
	v_mov_b32_e32 v55, v26
	v_mov_b32_e32 v56, v26
	v_mov_b32_e32 v57, v26
	v_mov_b32_e32 v2, v26
	v_mov_b32_e32 v3, v26
	v_mov_b32_e32 v4, v26
	v_mov_b32_e32 v5, v26
	v_mov_b32_e32 v14, v26
	v_mov_b32_e32 v15, v26
	v_mov_b32_e32 v16, v26
	v_mov_b32_e32 v17, v26
	v_mov_b32_e32 v30, v26
	v_mov_b32_e32 v31, v26
	v_mov_b32_e32 v32, v26
	v_mov_b32_e32 v33, v26
	v_mov_b32_e32 v34, v26
	v_mov_b32_e32 v35, v26
	v_mov_b32_e32 v36, v26
	v_mov_b32_e32 v37, v26
	v_mov_b32_e32 v42, v26
	v_mov_b32_e32 v43, v26
	v_mov_b32_e32 v44, v26
	v_mov_b32_e32 v45, v26
	v_mov_b32_e32 v50, v26
	v_mov_b32_e32 v51, v26
	v_mov_b32_e32 v52, v26
	v_mov_b32_e32 v53, v26
	v_mov_b32_e32 v58, v26
	v_mov_b32_e32 v59, v26
	v_mov_b32_e32 v60, v26
	v_mov_b32_e32 v61, v26
	v_mov_b32_e32 v62, v26
	v_mov_b32_e32 v63, v26
	v_mov_b32_e32 v64, v26
	v_mov_b32_e32 v65, v26
	v_mov_b32_e32 v66, v26
	v_mov_b32_e32 v67, v26
	v_mov_b32_e32 v68, v26
	v_mov_b32_e32 v69, v26
	v_mov_b32_e32 v70, v26
	v_mov_b32_e32 v71, v26
	v_mov_b32_e32 v72, v26
	v_mov_b32_e32 v73, v26
	v_mov_b32_e32 v82, v26
	v_mov_b32_e32 v83, v26
	v_mov_b32_e32 v84, v26
	v_mov_b32_e32 v85, v26
	v_mov_b32_e32 v86, v26
	v_mov_b32_e32 v87, v26
	v_mov_b32_e32 v88, v26
	v_mov_b32_e32 v89, v26
	v_mov_b32_e32 v98, v26
	v_mov_b32_e32 v99, v26
	v_mov_b32_e32 v100, v26
	v_mov_b32_e32 v101, v26
	v_mov_b32_e32 v102, v26
	v_mov_b32_e32 v103, v26
	v_mov_b32_e32 v104, v26
	v_mov_b32_e32 v105, v26
	v_mov_b32_e32 v114, v26
	v_mov_b32_e32 v115, v26
	v_mov_b32_e32 v116, v26
	v_mov_b32_e32 v117, v26
	v_mov_b32_e32 v118, v26
	v_mov_b32_e32 v119, v26
	v_mov_b32_e32 v120, v26
	v_mov_b32_e32 v121, v26
	v_mov_b32_e32 v74, v26
	v_mov_b32_e32 v75, v26
	v_mov_b32_e32 v76, v26
	v_mov_b32_e32 v77, v26
	v_mov_b32_e32 v78, v26
	v_mov_b32_e32 v79, v26
	v_mov_b32_e32 v80, v26
	v_mov_b32_e32 v81, v26
	v_mov_b32_e32 v90, v26
	v_mov_b32_e32 v91, v26
	v_mov_b32_e32 v92, v26
	v_mov_b32_e32 v93, v26
	v_mov_b32_e32 v94, v26
	v_mov_b32_e32 v95, v26
	v_mov_b32_e32 v96, v26
	v_mov_b32_e32 v97, v26
	v_mov_b32_e32 v106, v26
	v_mov_b32_e32 v107, v26
	v_mov_b32_e32 v108, v26
	v_mov_b32_e32 v109, v26
	v_mov_b32_e32 v110, v26
	v_mov_b32_e32 v111, v26
	v_mov_b32_e32 v112, v26
	v_mov_b32_e32 v113, v26
	v_mov_b32_e32 v122, v26
	v_mov_b32_e32 v123, v26
	v_mov_b32_e32 v124, v26
	v_mov_b32_e32 v125, v26
	v_mov_b32_e32 v126, v26
	v_mov_b32_e32 v127, v26
	v_mov_b32_e32 v128, v26
	v_mov_b32_e32 v129, v26
	v_mov_b32_e32 v22, v26
	v_mov_b32_e32 v23, v26
	v_mov_b32_e32 v24, v26
	v_mov_b32_e32 v25, v26
	v_mov_b32_e32 v18, v26
	v_mov_b32_e32 v19, v26
	v_mov_b32_e32 v20, v26
	v_mov_b32_e32 v21, v26
	v_mov_b32_e32 v10, v26
	v_mov_b32_e32 v11, v26
	v_mov_b32_e32 v12, v26
	v_mov_b32_e32 v13, v26
	v_mov_b32_e32 v6, v26
	v_mov_b32_e32 v7, v26
	v_mov_b32_e32 v8, v26
	v_mov_b32_e32 v9, v26
	.p2align 6
	s_nop 0
	s_nop 0
	s_nop 0
	s_nop 0
	s_nop 0
	s_nop 0
	s_nop 0
	s_nop 0

; #define PG8_STAGE(bufoff, gbase, voff) do { _Pragma("unroll") for (int _i = 0; _i < 2; ++_i) \
;         __builtin_amdgcn_global_load_lds((const unsigned*)((const char*)(gbase) + (voff)[_i]), (PG8_LAS unsigned*)(lds + (bufoff) + ldsw + _i * 8192), 16, 0, 0); } while (0)
; #define PG8_WAIT_V(n) asm volatile("s_waitcnt vmcnt(" #n ")" ::: "memory")
; #define PG8_BAR __builtin_amdgcn_s_barrier()
;     __device__ __forceinline__ Pre pre(const Unit& u, int wr, int fr) const { Pre p; const int rl0 = wr * 64 + fr;
; #pragma unroll
;         for (int ai = 0; ai < 2; ++ai)
; #pragma unroll
;             for (int m = 0; m < 4; ++m) { int slot = u.s0 + rl0 + ai * HALF + m * 16; slot = slot < u.cnt ? slot : u.cnt - 1; p.rs[ai][m] = lrs[u.e * 16384 + slot]; }
;         return p; }
; template <class Epi, class Sched, bool ALIGN_EPI = false>
; __device__ __forceinline__ void gemm_phase(PG8_LAS unsigned char* lds, const Gemm g, const Sched& S, const Epi& E) {
;     ...
;     PG8_STAGE(PG8_SB(0, 0), cB, voffB); PG8_STAGE(PG8_SB(0, 1), cB + hstep, voffB); PG8_STAGE(PG8_SA(0, 0), cA, vc0); PG8_STAGE(PG8_SA(0, 1), cA + hstepA, vc1);
;     if (wr == 1) PG8_BAR;
;     PG8_WAIT_V(2); PG8_BAR;
;     PG8_STAGE(PG8_SB(1, 0), cB + kstep, voffB); PG8_STAGE(PG8_SA(1, 0), cA + kstep, vc0); PG8_STAGE(PG8_SB(1, 1), cB + hstep + kstep, voffB);
;     PG8_WAIT_V(6); PG8_BAR;
.LBB0_1479:
	s_add_u32 s18, s36, 0x30800000
	v_lshlrev_b32_e32 v9, 2, v162
	s_addc_u32 s19, s37, 0
	v_lshl_or_b32 v166, s13, 6, v162
	v_lshl_or_b32 v8, v162, 6, v163
	s_lshl_b32 s13, s13, 13
	v_and_b32_e32 v9, 32, v9
	s_lshl_b32 s12, s12, 5
	v_bitop3_b32 v20, v8, s13, v9 bitop3:0xde
	s_and_b32 s40, s12, 0x60
	s_mov_b64 s[12:13], 0x80
	s_add_i32 m0, s25, 0x18000
	v_lshl_add_u64 v[4:5], v[4:5], 0, s[12:13]
	s_waitcnt vmcnt(2)
	s_barrier
	global_load_lds_dwordx4 v[4:5], off
	s_add_i32 m0, s25, 0x1a000
	s_add_u32 s48, s36, 0x3c800080
	v_lshl_add_u64 v[2:3], v[2:3], 0, s[12:13]
	s_addc_u32 s49, s37, 0
	s_add_i32 s41, s25, 0x8000
	global_load_lds_dwordx4 v[2:3], off
	v_lshl_add_u64 v[2:3], s[48:49], 0, v[148:149]
	s_mov_b32 m0, s41
	s_add_i32 s42, s25, 0xa000
	global_load_lds_dwordx4 v[2:3], off
	v_lshl_add_u64 v[2:3], s[48:49], 0, v[150:151]
	s_add_u32 s48, s10, 0x80080
	s_mov_b32 m0, s42
	s_addc_u32 s49, s11, 0
	global_load_lds_dwordx4 v[2:3], off
	s_add_i32 m0, s25, 0x1c000
	v_lshl_add_u64 v[2:3], s[48:49], 0, v[146:147]
	global_load_lds_dwordx4 v[2:3], off
	v_lshl_add_u64 v[2:3], s[48:49], 0, v[144:145]
	s_add_i32 m0, s25, 0x1e000
	v_add_u32_e32 v18, s46, v166
	global_load_lds_dwordx4 v[2:3], off
	v_min_i32_e32 v2, s44, v18
	v_add_u32_e32 v4, 16, v18
	v_add_u32_e32 v8, 32, v18
	v_add_u32_e32 v10, 48, v18
	v_add_u32_e32 v12, 0x80, v18
	v_add_u32_e32 v14, 0x90, v18
	v_add_u32_e32 v16, 0xa0, v18
	v_add_u32_e32 v18, 0xb0, v18
	v_add_u32_e32 v2, s43, v2
	v_min_i32_e32 v4, s44, v4
	v_min_i32_e32 v8, s44, v8
	v_min_i32_e32 v10, s44, v10
	v_min_i32_e32 v12, s44, v12
	v_min_i32_e32 v14, s44, v14
	v_min_i32_e32 v16, s44, v16
	v_min_i32_e32 v18, s44, v18
	v_ashrrev_i32_e32 v3, 31, v2
	v_add_u32_e32 v4, s43, v4
	v_add_u32_e32 v8, s43, v8
	v_add_u32_e32 v10, s43, v10
	v_add_u32_e32 v12, s43, v12
	v_add_u32_e32 v14, s43, v14
	v_add_u32_e32 v16, s43, v16
	v_add_u32_e32 v18, s43, v18
	v_lshl_add_u64 v[2:3], v[2:3], 2, s[18:19]
	v_ashrrev_i32_e32 v5, 31, v4
	v_ashrrev_i32_e32 v9, 31, v8
	v_ashrrev_i32_e32 v11, 31, v10
	v_ashrrev_i32_e32 v13, 31, v12
	v_ashrrev_i32_e32 v15, 31, v14
	v_ashrrev_i32_e32 v17, 31, v16
	v_ashrrev_i32_e32 v19, 31, v18
	s_waitcnt vmcnt(6)
	s_barrier
;     __device__ __forceinline__ Pre pre(const Unit& u, int wr, int fr) const { Pre p; const int rl0 = wr * 64 + fr;
; #pragma unroll
;         for (int ai = 0; ai < 2; ++ai)
; #pragma unroll
;             for (int m = 0; m < 4; ++m) { int slot = u.s0 + rl0 + ai * HALF + m * 16; slot = slot < u.cnt ? slot : u.cnt - 1; p.rs[ai][m] = lrs[u.e * 16384 + slot]; }
;         return p; }
; template <class Epi, class Sched, bool ALIGN_EPI = false>
; __device__ __forceinline__ void gemm_phase(PG8_LAS unsigned char* lds, const Gemm g, const Sched& S, const Epi& E) {
;     ...
;     Unit cur, nxt; int ui = 0;
;     if (!S.next(0, cur)) return;
;     f32x4 acc[2][2][4][2];
; #pragma unroll
;     for (int a = 0; a < 2; ++a)
; #pragma unroll
;         for (int b = 0; b < 2; ++b)
; #pragma unroll
;             for (int m = 0; m < 4; ++m)
; #pragma unroll
;                 for (int n = 0; n < 2; ++n) acc[a][b][m][n] = (f32x4){0.f, 0.f, 0.f, 0.f};
	v_lshl_add_u64 v[4:5], v[4:5], 2, s[18:19]
	v_lshl_add_u64 v[8:9], v[8:9], 2, s[18:19]
	v_lshl_add_u64 v[10:11], v[10:11], 2, s[18:19]
	v_lshl_add_u64 v[12:13], v[12:13], 2, s[18:19]
	v_lshl_add_u64 v[14:15], v[14:15], 2, s[18:19]
	v_lshl_add_u64 v[16:17], v[16:17], 2, s[18:19]
	v_lshl_add_u64 v[18:19], v[18:19], 2, s[18:19]
	global_load_dword v156, v[2:3], off
	global_load_dword v142, v[4:5], off
	global_load_dword v140, v[8:9], off
	global_load_dword v138, v[10:11], off
	global_load_dword v136, v[12:13], off
	global_load_dword v134, v[14:15], off
	global_load_dword v132, v[16:17], off
	global_load_dword v130, v[18:19], off
	s_add_u32 s14, s14, s45
	s_addc_u32 s15, s15, 0
	s_add_u32 s43, s14, 0xc800100
	v_lshl_or_b32 v21, s40, 7, v164
	s_mov_b64 s[16:17], 0x3c800080
	s_addc_u32 s44, s15, 0
	v_add3_u32 v2, v1, v7, v141
	v_mov_b32_e32 v3, v147
	s_add_i32 s48, 0, 0x10000
	s_add_i32 s50, 0, 0x14000
	s_add_i32 s52, 0, 0x18000
	s_add_i32 s14, 0, 0x1c000
	v_lshl_add_u64 v[158:159], v[2:3], 0, s[16:17]
	v_add3_u32 v2, v1, v6, v141
	v_add_u32_e32 v167, s48, v21
	v_add_u32_e32 v168, s50, v21
	s_add_i32 s48, s48, s54
	s_add_i32 s50, s50, s54
	v_add_u32_e32 v170, s52, v21
	s_add_i32 s52, s52, s54
	s_add_i32 s54, s14, s54
	v_mov_b32_e32 v153, v147
	v_mov_b32_e32 v155, v147
	v_lshl_add_u64 v[160:161], v[2:3], 0, s[16:17]
	s_mov_b32 s45, -2
	v_add_u32_e32 v169, 0, v20
	s_add_i32 s46, s25, 0xc000
	s_add_i32 s47, s25, 0xe000
	s_add_i32 s49, s48, 0x2000
	s_add_i32 s51, s50, 0x2000
	v_add_u32_e32 v171, s14, v21
	s_add_i32 s53, s52, 0x2000
	s_add_i32 s55, s54, 0x2000
	s_mov_b64 s[14:15], s[36:37]
	v_mov_b32_e32 v30, v147
	v_mov_b32_e32 v31, v147
	v_mov_b32_e32 v32, v147
	v_mov_b32_e32 v33, v147
	v_mov_b32_e32 v38, v147
	v_mov_b32_e32 v39, v147
	v_mov_b32_e32 v40, v147
	v_mov_b32_e32 v41, v147
	v_mov_b32_e32 v46, v147
	v_mov_b32_e32 v47, v147
	v_mov_b32_e32 v48, v147
	v_mov_b32_e32 v49, v147
	v_mov_b32_e32 v54, v147
	v_mov_b32_e32 v55, v147
	v_mov_b32_e32 v56, v147
	v_mov_b32_e32 v57, v147
	v_mov_b32_e32 v2, v147
	v_mov_b32_e32 v4, v147
	v_mov_b32_e32 v5, v147
	v_mov_b32_e32 v14, v147
	v_mov_b32_e32 v15, v147
	v_mov_b32_e32 v16, v147
	v_mov_b32_e32 v17, v147
	v_mov_b32_e32 v26, v147
	v_mov_b32_e32 v27, v147
	v_mov_b32_e32 v28, v147
	v_mov_b32_e32 v29, v147
	v_mov_b32_e32 v34, v147
	v_mov_b32_e32 v35, v147
	v_mov_b32_e32 v36, v147
	v_mov_b32_e32 v37, v147
	v_mov_b32_e32 v42, v147
	v_mov_b32_e32 v43, v147
	v_mov_b32_e32 v44, v147
	v_mov_b32_e32 v45, v147
	v_mov_b32_e32 v50, v147
	v_mov_b32_e32 v51, v147
	v_mov_b32_e32 v52, v147
	v_mov_b32_e32 v53, v147
	v_mov_b32_e32 v58, v147
	v_mov_b32_e32 v59, v147
	v_mov_b32_e32 v60, v147
	v_mov_b32_e32 v61, v147
	v_mov_b32_e32 v62, v147
	v_mov_b32_e32 v63, v147
	v_mov_b32_e32 v64, v147
	v_mov_b32_e32 v65, v147
	v_mov_b32_e32 v66, v147
	v_mov_b32_e32 v67, v147
	v_mov_b32_e32 v68, v147
	v_mov_b32_e32 v69, v147
	v_mov_b32_e32 v70, v147
	v_mov_b32_e32 v71, v147
	v_mov_b32_e32 v72, v147
	v_mov_b32_e32 v73, v147
	v_mov_b32_e32 v82, v147
	v_mov_b32_e32 v83, v147
	v_mov_b32_e32 v84, v147
	v_mov_b32_e32 v85, v147
	v_mov_b32_e32 v86, v147
	v_mov_b32_e32 v87, v147
	v_mov_b32_e32 v88, v147
	v_mov_b32_e32 v89, v147
	v_mov_b32_e32 v98, v147
	v_mov_b32_e32 v99, v147
	v_mov_b32_e32 v100, v147
	v_mov_b32_e32 v101, v147
	v_mov_b32_e32 v102, v147
	v_mov_b32_e32 v103, v147
	v_mov_b32_e32 v104, v147
	v_mov_b32_e32 v105, v147
	v_mov_b32_e32 v114, v147
	v_mov_b32_e32 v115, v147
	v_mov_b32_e32 v116, v147
	v_mov_b32_e32 v117, v147
	v_mov_b32_e32 v118, v147
	v_mov_b32_e32 v119, v147
	v_mov_b32_e32 v120, v147
	v_mov_b32_e32 v121, v147
	v_mov_b32_e32 v74, v147
	v_mov_b32_e32 v75, v147
	v_mov_b32_e32 v76, v147
	v_mov_b32_e32 v77, v147
	v_mov_b32_e32 v78, v147
	v_mov_b32_e32 v79, v147
	v_mov_b32_e32 v80, v147
	v_mov_b32_e32 v81, v147
	v_mov_b32_e32 v90, v147
	v_mov_b32_e32 v91, v147
	v_mov_b32_e32 v92, v147
	v_mov_b32_e32 v93, v147
	v_mov_b32_e32 v94, v147
	v_mov_b32_e32 v95, v147
	v_mov_b32_e32 v96, v147
	v_mov_b32_e32 v97, v147
	v_mov_b32_e32 v106, v147
	v_mov_b32_e32 v107, v147
	v_mov_b32_e32 v108, v147
	v_mov_b32_e32 v109, v147
	v_mov_b32_e32 v110, v147
	v_mov_b32_e32 v111, v147
	v_mov_b32_e32 v112, v147
	v_mov_b32_e32 v113, v147
	v_mov_b32_e32 v122, v147
	v_mov_b32_e32 v123, v147
	v_mov_b32_e32 v124, v147
	v_mov_b32_e32 v125, v147
	v_mov_b32_e32 v126, v147
	v_mov_b32_e32 v127, v147
	v_mov_b32_e32 v128, v147
	v_mov_b32_e32 v129, v147
	v_mov_b32_e32 v22, v147
	v_mov_b32_e32 v23, v147
	v_mov_b32_e32 v24, v147
	v_mov_b32_e32 v25, v147
	v_mov_b32_e32 v18, v147
	v_mov_b32_e32 v19, v147
	v_mov_b32_e32 v20, v147
	v_mov_b32_e32 v21, v147
	v_mov_b32_e32 v10, v147
	v_mov_b32_e32 v11, v147
	v_mov_b32_e32 v12, v147
	v_mov_b32_e32 v13, v147
	v_mov_b32_e32 v6, v147
	v_mov_b32_e32 v7, v147
	v_mov_b32_e32 v8, v147
	v_mov_b32_e32 v9, v147
	.p2align 6
	s_nop 0
	s_nop 0
	s_nop 0
	s_nop 0
	s_nop 0
	s_nop 0
	s_nop 0
	s_nop 0

; template <class Epi, class Sched, bool ALIGN_EPI = false>
; __device__ __forceinline__ void gemm_phase(PG8_LAS unsigned char* lds, const Gemm g, const Sched& S, const Epi& E) {
;     ...
;         const char* nA = Sched::GATHER ? (const char*)g.A : (has_next ? (const char*)g.A + (size_t)nxt.pm * tstep : cA); const char* nB = has_next ? (const char*)g.Bt + nxt.boff + (size_t)nxt.pn * tstep : cB;
;         for (int t = 0; t < nt; t += 2) {
;             const bool last = (t == nt - 2);
;             const char* a1 = cA + (size_t)(t + 1) * kstep;
;             const char* a2 = last ? nA : cA + (size_t)(t + 2) * kstep; const char* b2 = last ? nB : cB + (size_t)(t + 2) * kstep;
;             const char* a3 = a2 + kstep; const char* b3 = b2 + kstep;
;             unsigned w0[2], w1[2];
; #pragma unroll
;             for (int i = 0; i < 2; ++i) { w0[i] = (Sched::GATHER && last) ? vn0[i] : vc0[i]; w1[i] = (Sched::GATHER && last) ? vn1[i] : vc1[i]; }
;             if (last && has_next) S.a_ready(nxt);
;             PG8_LDB(B0, 0, 0); PG8_LDB(B1, 0, 1); PG8_SCHED; PG8_LDA(At, 0, 0); PG8_STAGE(PG8_SA(1, 1), a1 + hstepA, vc1);
;             PG8_WAIT_V(8); PG8_WAIT_L(0); PG8_BAR; PG8_MMA(0, 0, At, B0); PG8_MMA(0, 1, At, B1); PG8_BAR; PG8_SCHED;
;             PG8_LDA(At, 0, 1); PG8_STAGE(PG8_SB(0, 0), b2, voffB); PG8_STAGE(PG8_SB(0, 1), b2 + hstep, voffB); PG8_STAGE(PG8_SA(0, 0), a2, w0);
;             PG8_WAIT_V(8); PG8_WAIT_L(0); PG8_BAR; PG8_MMA(1, 0, At, B0); PG8_MMA(1, 1, At, B1); PG8_BAR; PG8_SCHED;
;             PG8_LDB(B0, 1, 0); PG8_LDB(B1, 1, 1); PG8_SCHED; PG8_LDA(At, 1, 0); PG8_STAGE(PG8_SA(0, 1), a2 + hstepA, w1);
;             PG8_WAIT_V(8); PG8_WAIT_L(0); PG8_BAR; PG8_MMA(0, 0, At, B0); PG8_MMA(0, 1, At, B1); PG8_BAR; PG8_SCHED;
;             PG8_LDA(At, 1, 1); PG8_STAGE(PG8_SB(1, 0), b3, voffB); PG8_STAGE(PG8_SB(1, 1), b3 + hstep, voffB); PG8_STAGE(PG8_SA(1, 0), a3, w0);
;             PG8_WAIT_V(8); PG8_WAIT_L(0); PG8_BAR; PG8_MMA(1, 0, At, B0); PG8_MMA(1, 1, At, B1); PG8_BAR; PG8_SCHED;
;             if constexpr (Epi::KSCALE) { if (((t + 2) & 7) == 0 && t + 2 < nt) { E.kscale(acc, pf, ((t + 2) >> 3) - 1, wr, fr); PG8_SCHED; } }
;         }
;         if constexpr (ALIGN_EPI) { if (wr == 0) PG8_BAR; }
;         if constexpr (!Epi::AFTER_DRAIN) { E(acc, cur, wr, wc, fr, fq, pf); S.done(cur); }
;         if (!has_next) break;
; #pragma unroll
.LBB0_1497:
	s_ashr_i32 s41, s40, 31
	s_lshl_b64 s[48:49], s[40:41], 18
	s_add_u32 s48, s8, s48
	s_addc_u32 s49, s9, s49
	s_and_b64 s[50:51], s[46:47], exec
	s_cselect_b32 s41, s49, s59
	s_cselect_b32 s53, s48, s58
	s_add_u32 s60, s3, s44
	s_addc_u32 s61, s35, s45
	s_ashr_i32 s43, s42, 31
	s_lshl_b64 s[50:51], s[42:43], 18
	s_add_u32 s50, s60, s50
	s_addc_u32 s51, s61, s51
	s_and_b64 s[60:61], s[46:47], exec
	s_cselect_b32 s43, s51, s57
	s_cselect_b32 s84, s50, s56
	s_add_u32 s85, s56, 0x100
	s_addc_u32 s86, s57, 0
	s_add_u32 s56, s58, 0x20080
	v_mov_b32_e32 v2, 0
	s_addc_u32 s57, s59, 0
	s_mov_b32 s87, -2
	v_mov_b32_e32 v3, v2
	v_mov_b32_e32 v4, v2
	v_mov_b32_e32 v5, v2
	v_mov_b32_e32 v6, v2
	v_mov_b32_e32 v7, v2
	v_mov_b32_e32 v8, v2
	v_mov_b32_e32 v9, v2
	v_mov_b32_e32 v10, v2
	v_mov_b32_e32 v11, v2
	v_mov_b32_e32 v12, v2
	v_mov_b32_e32 v13, v2
	v_mov_b32_e32 v14, v2
	v_mov_b32_e32 v15, v2
	v_mov_b32_e32 v16, v2
	v_mov_b32_e32 v17, v2
	v_mov_b32_e32 v26, v2
	v_mov_b32_e32 v27, v2
	v_mov_b32_e32 v28, v2
	v_mov_b32_e32 v29, v2
	v_mov_b32_e32 v30, v2
	v_mov_b32_e32 v31, v2
	v_mov_b32_e32 v32, v2
	v_mov_b32_e32 v33, v2
	v_mov_b32_e32 v42, v2
	v_mov_b32_e32 v43, v2
	v_mov_b32_e32 v44, v2
	v_mov_b32_e32 v45, v2
	v_mov_b32_e32 v54, v2
	v_mov_b32_e32 v55, v2
	v_mov_b32_e32 v56, v2
	v_mov_b32_e32 v57, v2
	v_mov_b32_e32 v58, v2
	v_mov_b32_e32 v59, v2
	v_mov_b32_e32 v60, v2
	v_mov_b32_e32 v61, v2
	v_mov_b32_e32 v62, v2
	v_mov_b32_e32 v63, v2
	v_mov_b32_e32 v64, v2
	v_mov_b32_e32 v65, v2
	v_mov_b32_e32 v78, v2
	v_mov_b32_e32 v79, v2
	v_mov_b32_e32 v80, v2
	v_mov_b32_e32 v81, v2
	v_mov_b32_e32 v86, v2
	v_mov_b32_e32 v87, v2
	v_mov_b32_e32 v88, v2
	v_mov_b32_e32 v89, v2
	v_mov_b32_e32 v94, v2
	v_mov_b32_e32 v95, v2
	v_mov_b32_e32 v96, v2
	v_mov_b32_e32 v97, v2
	v_mov_b32_e32 v102, v2
	v_mov_b32_e32 v103, v2
	v_mov_b32_e32 v104, v2
	v_mov_b32_e32 v105, v2
	v_mov_b32_e32 v110, v2
	v_mov_b32_e32 v111, v2
	v_mov_b32_e32 v112, v2
	v_mov_b32_e32 v113, v2
	v_mov_b32_e32 v118, v2
	v_mov_b32_e32 v119, v2
	v_mov_b32_e32 v120, v2
	v_mov_b32_e32 v121, v2
	v_mov_b32_e32 v74, v2
	v_mov_b32_e32 v75, v2
	v_mov_b32_e32 v76, v2
	v_mov_b32_e32 v77, v2
	v_mov_b32_e32 v82, v2
	v_mov_b32_e32 v83, v2
	v_mov_b32_e32 v84, v2
	v_mov_b32_e32 v85, v2
	v_mov_b32_e32 v90, v2
	v_mov_b32_e32 v91, v2
	v_mov_b32_e32 v92, v2
	v_mov_b32_e32 v93, v2
	v_mov_b32_e32 v98, v2
	v_mov_b32_e32 v99, v2
	v_mov_b32_e32 v100, v2
	v_mov_b32_e32 v101, v2
	v_mov_b32_e32 v106, v2
	v_mov_b32_e32 v107, v2
	v_mov_b32_e32 v108, v2
	v_mov_b32_e32 v109, v2
	v_mov_b32_e32 v114, v2
	v_mov_b32_e32 v115, v2
	v_mov_b32_e32 v116, v2
	v_mov_b32_e32 v117, v2
	v_mov_b32_e32 v122, v2
	v_mov_b32_e32 v123, v2
	v_mov_b32_e32 v124, v2
	v_mov_b32_e32 v125, v2
	v_mov_b32_e32 v126, v2
	v_mov_b32_e32 v127, v2
	v_mov_b32_e32 v128, v2
	v_mov_b32_e32 v129, v2
	v_mov_b32_e32 v70, v2
	v_mov_b32_e32 v71, v2
	v_mov_b32_e32 v72, v2
	v_mov_b32_e32 v73, v2
	v_mov_b32_e32 v66, v2
	v_mov_b32_e32 v67, v2
	v_mov_b32_e32 v68, v2
	v_mov_b32_e32 v69, v2
	v_mov_b32_e32 v50, v2
	v_mov_b32_e32 v51, v2
	v_mov_b32_e32 v52, v2
	v_mov_b32_e32 v53, v2
	v_mov_b32_e32 v46, v2
	v_mov_b32_e32 v47, v2
	v_mov_b32_e32 v48, v2
	v_mov_b32_e32 v49, v2
	v_mov_b32_e32 v38, v2
	v_mov_b32_e32 v39, v2
	v_mov_b32_e32 v40, v2
	v_mov_b32_e32 v41, v2
	v_mov_b32_e32 v34, v2
	v_mov_b32_e32 v35, v2
	v_mov_b32_e32 v36, v2
	v_mov_b32_e32 v37, v2
	v_mov_b32_e32 v22, v2
	v_mov_b32_e32 v23, v2
	v_mov_b32_e32 v24, v2
	v_mov_b32_e32 v25, v2
	v_mov_b32_e32 v18, v2
	v_mov_b32_e32 v19, v2
	v_mov_b32_e32 v20, v2
	v_mov_b32_e32 v21, v2
	.p2align 6
	s_nop 0
	s_nop 0
	s_nop 0
	s_nop 0
	s_nop 0
	s_nop 0
	s_nop 0
	s_nop 0

; template <class Epi, class Sched, bool ALIGN_EPI = false>
; __device__ __forceinline__ void gemm_phase(PG8_LAS unsigned char* lds, const Gemm g, const Sched& S, const Epi& E) {
;     ...
;         const char* nA = Sched::GATHER ? (const char*)g.A : (has_next ? (const char*)g.A + (size_t)nxt.pm * tstep : cA); const char* nB = has_next ? (const char*)g.Bt + nxt.boff + (size_t)nxt.pn * tstep : cB;
;         for (int t = 0; t < nt; t += 2) {
;             const bool last = (t == nt - 2);
;             const char* a1 = cA + (size_t)(t + 1) * kstep;
;             const char* a2 = last ? nA : cA + (size_t)(t + 2) * kstep; const char* b2 = last ? nB : cB + (size_t)(t + 2) * kstep;
;             const char* a3 = a2 + kstep; const char* b3 = b2 + kstep;
;             unsigned w0[2], w1[2];
; #pragma unroll
;             for (int i = 0; i < 2; ++i) { w0[i] = (Sched::GATHER && last) ? vn0[i] : vc0[i]; w1[i] = (Sched::GATHER && last) ? vn1[i] : vc1[i]; }
;             if (last && has_next) S.a_ready(nxt);
;             PG8_LDB(B0, 0, 0); PG8_LDB(B1, 0, 1); PG8_SCHED; PG8_LDA(At, 0, 0); PG8_STAGE(PG8_SA(1, 1), a1 + hstepA, vc1);
;             PG8_WAIT_V(8); PG8_WAIT_L(0); PG8_BAR; PG8_MMA(0, 0, At, B0); PG8_MMA(0, 1, At, B1); PG8_BAR; PG8_SCHED;
;             PG8_LDA(At, 0, 1); PG8_STAGE(PG8_SB(0, 0), b2, voffB); PG8_STAGE(PG8_SB(0, 1), b2 + hstep, voffB); PG8_STAGE(PG8_SA(0, 0), a2, w0);
;             PG8_WAIT_V(8); PG8_WAIT_L(0); PG8_BAR; PG8_MMA(1, 0, At, B0); PG8_MMA(1, 1, At, B1); PG8_BAR; PG8_SCHED;
;             PG8_LDB(B0, 1, 0); PG8_LDB(B1, 1, 1); PG8_SCHED; PG8_LDA(At, 1, 0); PG8_STAGE(PG8_SA(0, 1), a2 + hstepA, w1);
;             PG8_WAIT_V(8); PG8_WAIT_L(0); PG8_BAR; PG8_MMA(0, 0, At, B0); PG8_MMA(0, 1, At, B1); PG8_BAR; PG8_SCHED;
;             PG8_LDA(At, 1, 1); PG8_STAGE(PG8_SB(1, 0), b3, voffB); PG8_STAGE(PG8_SB(1, 1), b3 + hstep, voffB); PG8_STAGE(PG8_SA(1, 0), a3, w0);
;             PG8_WAIT_V(8); PG8_WAIT_L(0); PG8_BAR; PG8_MMA(1, 0, At, B0); PG8_MMA(1, 1, At, B1); PG8_BAR; PG8_SCHED;
;             if constexpr (Epi::KSCALE) { if (((t + 2) & 7) == 0 && t + 2 < nt) { E.kscale(acc, pf, ((t + 2) >> 3) - 1, wr, fr); PG8_SCHED; } }
;         }
;         if constexpr (ALIGN_EPI) { if (wr == 0) PG8_BAR; }
;         if constexpr (!Epi::AFTER_DRAIN) { E(acc, cur, wr, wc, fr, fq, pf); S.done(cur); }
;         if (!has_next) break;
; #pragma unroll
.LBB0_1600:
	s_ashr_i32 s25, s24, 31
	s_lshl_b64 s[46:47], s[24:25], 18
	s_add_u32 s46, s58, s46
	s_addc_u32 s47, s59, s47
	s_and_b64 s[50:51], s[48:49], exec
	s_cselect_b32 s25, s47, s55
	s_cselect_b32 s43, s46, s54
	s_add_u32 s56, s60, s40
	s_addc_u32 s57, s61, s41
	s_ashr_i32 s27, s26, 31
	s_lshl_b64 s[50:51], s[26:27], 18
	s_add_u32 s50, s56, s50
	s_addc_u32 s51, s57, s51
	s_and_b64 s[56:57], s[48:49], exec
	s_cselect_b32 s27, s51, s53
	s_cselect_b32 s84, s50, s52
	s_add_u32 s85, s52, 0x100
	s_addc_u32 s86, s53, 0
	s_add_u32 s52, s54, 0x20080
	v_mov_b32_e32 v2, 0
	s_addc_u32 s53, s55, 0
	s_mov_b32 s87, -2
	v_mov_b32_e32 v3, v2
	v_mov_b32_e32 v4, v2
	v_mov_b32_e32 v5, v2
	v_mov_b32_e32 v6, v2
	v_mov_b32_e32 v7, v2
	v_mov_b32_e32 v8, v2
	v_mov_b32_e32 v9, v2
	v_mov_b32_e32 v10, v2
	v_mov_b32_e32 v11, v2
	v_mov_b32_e32 v12, v2
	v_mov_b32_e32 v13, v2
	v_mov_b32_e32 v14, v2
	v_mov_b32_e32 v15, v2
	v_mov_b32_e32 v16, v2
	v_mov_b32_e32 v17, v2
	v_mov_b32_e32 v26, v2
	v_mov_b32_e32 v27, v2
	v_mov_b32_e32 v28, v2
	v_mov_b32_e32 v29, v2
	v_mov_b32_e32 v30, v2
	v_mov_b32_e32 v31, v2
	v_mov_b32_e32 v32, v2
	v_mov_b32_e32 v33, v2
	v_mov_b32_e32 v42, v2
	v_mov_b32_e32 v43, v2
	v_mov_b32_e32 v44, v2
	v_mov_b32_e32 v45, v2
	v_mov_b32_e32 v54, v2
	v_mov_b32_e32 v55, v2
	v_mov_b32_e32 v56, v2
	v_mov_b32_e32 v57, v2
	v_mov_b32_e32 v58, v2
	v_mov_b32_e32 v59, v2
	v_mov_b32_e32 v60, v2
	v_mov_b32_e32 v61, v2
	v_mov_b32_e32 v62, v2
	v_mov_b32_e32 v63, v2
	v_mov_b32_e32 v64, v2
	v_mov_b32_e32 v65, v2
	v_mov_b32_e32 v78, v2
	v_mov_b32_e32 v79, v2
	v_mov_b32_e32 v80, v2
	v_mov_b32_e32 v81, v2
	v_mov_b32_e32 v86, v2
	v_mov_b32_e32 v87, v2
	v_mov_b32_e32 v88, v2
	v_mov_b32_e32 v89, v2
	v_mov_b32_e32 v94, v2
	v_mov_b32_e32 v95, v2
	v_mov_b32_e32 v96, v2
	v_mov_b32_e32 v97, v2
	v_mov_b32_e32 v102, v2
	v_mov_b32_e32 v103, v2
	v_mov_b32_e32 v104, v2
	v_mov_b32_e32 v105, v2
	v_mov_b32_e32 v110, v2
	v_mov_b32_e32 v111, v2
	v_mov_b32_e32 v112, v2
	v_mov_b32_e32 v113, v2
	v_mov_b32_e32 v118, v2
	v_mov_b32_e32 v119, v2
	v_mov_b32_e32 v120, v2
	v_mov_b32_e32 v121, v2
	v_mov_b32_e32 v74, v2
	v_mov_b32_e32 v75, v2
	v_mov_b32_e32 v76, v2
	v_mov_b32_e32 v77, v2
	v_mov_b32_e32 v82, v2
	v_mov_b32_e32 v83, v2
	v_mov_b32_e32 v84, v2
	v_mov_b32_e32 v85, v2
	v_mov_b32_e32 v90, v2
	v_mov_b32_e32 v91, v2
	v_mov_b32_e32 v92, v2
	v_mov_b32_e32 v93, v2
	v_mov_b32_e32 v98, v2
	v_mov_b32_e32 v99, v2
	v_mov_b32_e32 v100, v2
	v_mov_b32_e32 v101, v2
	v_mov_b32_e32 v106, v2
	v_mov_b32_e32 v107, v2
	v_mov_b32_e32 v108, v2
	v_mov_b32_e32 v109, v2
	v_mov_b32_e32 v114, v2
	v_mov_b32_e32 v115, v2
	v_mov_b32_e32 v116, v2
	v_mov_b32_e32 v117, v2
	v_mov_b32_e32 v122, v2
	v_mov_b32_e32 v123, v2
	v_mov_b32_e32 v124, v2
	v_mov_b32_e32 v125, v2
	v_mov_b32_e32 v126, v2
	v_mov_b32_e32 v127, v2
	v_mov_b32_e32 v128, v2
	v_mov_b32_e32 v129, v2
	v_mov_b32_e32 v70, v2
	v_mov_b32_e32 v71, v2
	v_mov_b32_e32 v72, v2
	v_mov_b32_e32 v73, v2
	v_mov_b32_e32 v66, v2
	v_mov_b32_e32 v67, v2
	v_mov_b32_e32 v68, v2
	v_mov_b32_e32 v69, v2
	v_mov_b32_e32 v50, v2
	v_mov_b32_e32 v51, v2
	v_mov_b32_e32 v52, v2
	v_mov_b32_e32 v53, v2
	v_mov_b32_e32 v46, v2
	v_mov_b32_e32 v47, v2
	v_mov_b32_e32 v48, v2
	v_mov_b32_e32 v49, v2
	v_mov_b32_e32 v38, v2
	v_mov_b32_e32 v39, v2
	v_mov_b32_e32 v40, v2
	v_mov_b32_e32 v41, v2
	v_mov_b32_e32 v34, v2
	v_mov_b32_e32 v35, v2
	v_mov_b32_e32 v36, v2
	v_mov_b32_e32 v37, v2
	v_mov_b32_e32 v22, v2
	v_mov_b32_e32 v23, v2
	v_mov_b32_e32 v24, v2
	v_mov_b32_e32 v25, v2
	v_mov_b32_e32 v18, v2
	v_mov_b32_e32 v19, v2
	v_mov_b32_e32 v20, v2
	v_mov_b32_e32 v21, v2
	.p2align 6
	s_nop 0
	s_nop 0
	s_nop 0
	s_nop 0
	s_nop 0
	s_nop 0
	s_nop 0
	s_nop 0
